# round-0 q/k tiles touch (prefetch into the memory-side cache) the ve region of their partner round-1 v tile from the VALU-bound epilogue, after its last vmcnt wait
# speedup vs baseline: 1.0029x; 1.0012x over previous
.LBB2_16:
	s_load_dwordx2 s[50:51], s[0:1], 0x28
	s_or_b32 s52, s2, 0x20
	s_and_b32 s53, s52, 7
	s_lshl_b32 s53, s53, 5
	s_lshr_b32 s54, s52, 3
	s_add_i32 s53, s53, s54
	s_lshr_b32 s54, s53, 6
	s_lshl_b32 s54, s54, 3
	s_and_b32 s55, s53, 7
	s_add_i32 s54, s54, s55
	s_bfe_u32 s55, s53, 0x30003
	s_lshl_b32 s54, s54, 20
	s_lshl_b32 s55, s55, 10
	s_add_i32 s54, s54, s55
	s_and_b32 s55, s2, 0x20
	v_lshlrev_b32_e32 v1, 4, v0
	v_and_b32_e32 v2, 32, v0
	v_lshrrev_b32_e32 v3, 3, v0
	v_bfe_u32 v4, v0, 2, 4
	v_bitop3_b32 v1, v1, v2, 48 bitop3:0x6c
	v_and_or_b32 v5, v3, 48, v4
	v_and_or_b32 v1, v0, 64, v1
	v_lshl_or_b32 v135, v5, 12, v1
	v_lshlrev_b32_e32 v2, 1, v4
	v_and_b32_e32 v3, 32, v3
	v_bfe_u32 v5, v0, 7, 1
	v_or3_b32 v2, v3, v2, v5
	v_readfirstlane_b32 s10, v0
	v_lshl_or_b32 v137, v2, 12, v1
	v_bfe_u32 v2, v0, 3, 25
	s_lshl_b32 s3, s2, 5
	v_or_b32_e32 v3, 64, v2
	s_movk_i32 s11, 0x70
	s_lshl_b32 s10, s10, 4
	s_lshr_b32 s39, s2, 3
	s_lshl_b32 s6, s2, 1
	s_and_b32 s40, s3, 0x60
	v_and_or_b32 v3, v3, s11, v4
	s_and_b32 s35, s10, 0x7ffffc00
	s_and_b32 s6, s6, 8
	s_or_b32 s3, s40, s39
	s_bfe_u32 s41, s2, 0x30003
	v_lshl_or_b32 v136, v3, 12, v1
	v_lshlrev_b32_e32 v3, 1, v3
	s_add_i32 s23, s35, 0
	s_or_b32 s21, s6, s41
	s_mov_b32 s7, 0x20000
	s_mov_b32 s6, 0x1000000
	s_and_b32 s9, s9, 0xffff
	v_bitop3_b32 v2, v2, 32, 64 bitop3:0xc8
	v_and_b32_e32 v3, 0x9e, v3
	s_lshl_b32 s11, s3, 17
	s_add_i32 s24, s23, 0x10000
	s_mov_b32 s12, s8
	s_mov_b32 s13, s9
	s_mov_b32 s14, s6
	s_mov_b32 s15, s7
	v_or3_b32 v2, v2, v3, v5
	s_and_b32 s20, s11, 0xfff00000
	s_mov_b32 m0, s24
	s_add_i32 s25, s23, 0x12000
	v_lshl_or_b32 v140, v2, 12, v1
	buffer_load_dwordx4 v137, s[12:15], s20 offen lds
	s_mov_b32 m0, s25
	s_and_b32 s5, s5, 0xffff
	buffer_load_dwordx4 v140, s[12:15], s20 offen lds
	s_lshl_b32 s22, s21, 20
	s_mov_b32 m0, s23
	s_add_i32 s26, s23, 0x2000
	buffer_load_dwordx4 v135, s[4:7], s22 offen lds
	s_mov_b32 m0, s26
	s_add_i32 s27, s23, 0x14000
	buffer_load_dwordx4 v136, s[4:7], s22 offen lds
	s_or_b32 s10, s20, 0x40000
	s_mov_b32 m0, s27
	s_add_i32 s28, s23, 0x16000
	buffer_load_dwordx4 v137, s[12:15], s10 offen lds
	s_mov_b32 m0, s28
	s_add_i32 s29, s23, 0x4000
	buffer_load_dwordx4 v140, s[12:15], s10 offen lds
	s_or_b32 s10, s22, 0x80000
	s_mov_b32 m0, s29
	s_add_i32 s30, s23, 0x6000
	buffer_load_dwordx4 v135, s[4:7], s10 offen lds
	s_mov_b32 m0, s30
	v_lshrrev_b32_e32 v154, 8, v0
	buffer_load_dwordx4 v136, s[4:7], s10 offen lds
	s_mov_b32 s10, s6
	s_mov_b32 s11, s7
	s_mov_b32 s31, 0
	v_cmp_eq_u32_e32 vcc, 1, v154
	s_and_saveexec_b64 s[6:7], vcc
	s_cbranch_execz .LBB2_18
	s_barrier

.LBB2_22:
	s_or_b64 exec, exec, s[0:1]
	v_fma_f32 v133, v118, v118, 0
	v_fmac_f32_e32 v133, v114, v114
	v_fmac_f32_e32 v133, v122, v122
	v_fmac_f32_e32 v133, v126, v126
	v_lshrrev_b32_e32 v131, 2, v0
	v_and_or_b32 v187, v131, 12, v141
	v_add_f32_dpp v133, v133, v133 row_ror:8 row_mask:0xf bank_mask:0xf bound_ctrl:1
	v_lshl_add_u32 v132, v1, 2, 0
	v_lshl_add_u32 v134, v187, 4, v132
	v_add_f32_dpp v133, v133, v133 row_ror:4 row_mask:0xf bank_mask:0xf bound_ctrl:1
	s_waitcnt vmcnt(0)
	s_barrier
	v_lshrrev_b32_e32 v252, 2, v0
	v_and_b32_e32 v253, 3, v0
	v_lshlrev_b32_e32 v252, 13, v252
	v_lshl_or_b32 v252, v253, 8, v252
	v_add_f32_dpp v133, v133, v133 quad_perm:[2,3,0,1] row_mask:0xf bank_mask:0xf bound_ctrl:1
	v_or_b32_e32 v190, 1, v187
	s_nop 0
	v_add_f32_dpp v133, v133, v133 quad_perm:[1,0,3,2] row_mask:0xf bank_mask:0xf bound_ctrl:1
	ds_write_b32 v134, v133
	v_fma_f32 v133, v119, v119, 0
	v_fmac_f32_e32 v133, v115, v115
	v_fmac_f32_e32 v133, v123, v123
	v_fmac_f32_e32 v133, v127, v127
	v_lshl_add_u32 v134, v190, 4, v132
	v_or_b32_e32 v189, 2, v187
	v_add_f32_dpp v133, v133, v133 row_ror:8 row_mask:0xf bank_mask:0xf bound_ctrl:1
	v_or_b32_e32 v188, 3, v187
	v_or_b32_e32 v183, 16, v187
	v_add_f32_dpp v133, v133, v133 row_ror:4 row_mask:0xf bank_mask:0xf bound_ctrl:1
	v_or_b32_e32 v186, 17, v187
	v_or_b32_e32 v185, 18, v187
	v_add_f32_dpp v133, v133, v133 quad_perm:[2,3,0,1] row_mask:0xf bank_mask:0xf bound_ctrl:1
	v_or_b32_e32 v184, 19, v187
	v_or_b32_e32 v178, 32, v187
	v_add_f32_dpp v133, v133, v133 quad_perm:[1,0,3,2] row_mask:0xf bank_mask:0xf bound_ctrl:1
	ds_write_b32 v134, v133
	v_fma_f32 v133, v120, v120, 0
	v_fmac_f32_e32 v133, v116, v116
	v_fmac_f32_e32 v133, v124, v124
	v_fmac_f32_e32 v133, v128, v128
	v_lshl_add_u32 v134, v189, 4, v132
	v_or_b32_e32 v181, 33, v187
	v_add_f32_dpp v133, v133, v133 row_ror:8 row_mask:0xf bank_mask:0xf bound_ctrl:1
	v_or_b32_e32 v180, 34, v187
	v_or_b32_e32 v179, 35, v187
	v_add_f32_dpp v133, v133, v133 row_ror:4 row_mask:0xf bank_mask:0xf bound_ctrl:1
	v_or_b32_e32 v174, 48, v187
	v_or_b32_e32 v177, 49, v187
	v_add_f32_dpp v133, v133, v133 quad_perm:[2,3,0,1] row_mask:0xf bank_mask:0xf bound_ctrl:1
	v_or_b32_e32 v176, 50, v187
	v_or_b32_e32 v175, 51, v187
	v_add_f32_dpp v133, v133, v133 quad_perm:[1,0,3,2] row_mask:0xf bank_mask:0xf bound_ctrl:1
	ds_write_b32 v134, v133
	v_fma_f32 v133, v121, v121, 0
	v_fmac_f32_e32 v133, v117, v117
	v_fmac_f32_e32 v133, v125, v125
	v_fmac_f32_e32 v133, v129, v129
	v_lshl_add_u32 v134, v188, 4, v132
	v_or_b32_e32 v173, 0x80, v187
	v_add_f32_dpp v133, v133, v133 row_ror:8 row_mask:0xf bank_mask:0xf bound_ctrl:1
	v_add_u32_e32 v172, 0x81, v187
	v_add_u32_e32 v171, 0x82, v187
	v_add_f32_dpp v133, v133, v133 row_ror:4 row_mask:0xf bank_mask:0xf bound_ctrl:1
	v_add_u32_e32 v170, 0x83, v187
	v_add_u32_e32 v166, 0x90, v187
	v_add_f32_dpp v133, v133, v133 quad_perm:[2,3,0,1] row_mask:0xf bank_mask:0xf bound_ctrl:1
	v_add_u32_e32 v169, 0x91, v187
	v_add_u32_e32 v168, 0x92, v187
	v_add_f32_dpp v133, v133, v133 quad_perm:[1,0,3,2] row_mask:0xf bank_mask:0xf bound_ctrl:1
	ds_write_b32 v134, v133
	v_fma_f32 v133, v102, v102, 0
	v_fmac_f32_e32 v133, v98, v98
	v_fmac_f32_e32 v133, v106, v106
	v_fmac_f32_e32 v133, v110, v110
	v_lshl_add_u32 v134, v183, 4, v132
	v_add_u32_e32 v167, 0x93, v187
	v_add_f32_dpp v133, v133, v133 row_ror:8 row_mask:0xf bank_mask:0xf bound_ctrl:1
	v_add_u32_e32 v160, 0xa0, v187
	v_add_u32_e32 v165, 0xa1, v187
	v_add_f32_dpp v133, v133, v133 row_ror:4 row_mask:0xf bank_mask:0xf bound_ctrl:1
	v_add_u32_e32 v164, 0xa2, v187
	v_add_u32_e32 v163, 0xa3, v187
	v_add_f32_dpp v133, v133, v133 quad_perm:[2,3,0,1] row_mask:0xf bank_mask:0xf bound_ctrl:1
	v_add_u32_e32 v153, 0xb0, v187
	v_add_u32_e32 v159, 0xb1, v187
	v_add_f32_dpp v133, v133, v133 quad_perm:[1,0,3,2] row_mask:0xf bank_mask:0xf bound_ctrl:1
	ds_write_b32 v134, v133
	v_fma_f32 v133, v103, v103, 0
	v_fmac_f32_e32 v133, v99, v99
	v_fmac_f32_e32 v133, v107, v107
	v_fmac_f32_e32 v133, v111, v111
	v_lshl_add_u32 v134, v186, 4, v132
	v_add_u32_e32 v157, 0xb2, v187
	v_add_f32_dpp v133, v133, v133 row_ror:8 row_mask:0xf bank_mask:0xf bound_ctrl:1
	v_add_u32_e32 v156, 0xb3, v187
	v_bfe_u32 v136, v0, 6, 1
	v_add_f32_dpp v133, v133, v133 row_ror:4 row_mask:0xf bank_mask:0xf bound_ctrl:1
	s_lshl_b32 s2, s21, 8
	v_lshrrev_b32_e32 v152, 4, v0
	v_add_f32_dpp v133, v133, v133 quad_perm:[2,3,0,1] row_mask:0xf bank_mask:0xf bound_ctrl:1
	v_mov_b32_e32 v131, 0
	v_cmp_eq_u32_e32 vcc, 0, v136
	v_add_f32_dpp v133, v133, v133 quad_perm:[1,0,3,2] row_mask:0xf bank_mask:0xf bound_ctrl:1
	ds_write_b32 v134, v133
	v_fma_f32 v133, v104, v104, 0
	v_fmac_f32_e32 v133, v100, v100
	v_fmac_f32_e32 v133, v108, v108
	v_fmac_f32_e32 v133, v112, v112
	v_lshl_add_u32 v134, v185, 4, v132
	v_mov_b32_e32 v142, 1.0
	v_add_f32_dpp v133, v133, v133 row_ror:8 row_mask:0xf bank_mask:0xf bound_ctrl:1
	v_mov_b32_e32 v143, 1.0
	v_mov_b32_e32 v144, 0
	v_add_f32_dpp v133, v133, v133 row_ror:4 row_mask:0xf bank_mask:0xf bound_ctrl:1
	v_mov_b32_e32 v145, 0
	v_mov_b32_e32 v135, 0
	v_add_f32_dpp v133, v133, v133 quad_perm:[2,3,0,1] row_mask:0xf bank_mask:0xf bound_ctrl:1
	v_mov_b32_e32 v138, 1.0
	v_mov_b32_e32 v139, 1.0
	v_add_f32_dpp v133, v133, v133 quad_perm:[1,0,3,2] row_mask:0xf bank_mask:0xf bound_ctrl:1
	ds_write_b32 v134, v133
	v_fma_f32 v133, v105, v105, 0
	v_fmac_f32_e32 v133, v101, v101
	v_fmac_f32_e32 v133, v109, v109
	v_fmac_f32_e32 v133, v113, v113
	v_lshl_add_u32 v134, v184, 4, v132
	v_mov_b32_e32 v140, 0
	v_add_f32_dpp v133, v133, v133 row_ror:8 row_mask:0xf bank_mask:0xf bound_ctrl:1
	v_mov_b32_e32 v141, 0
	v_mov_b32_e32 v146, 1.0
	v_add_f32_dpp v133, v133, v133 row_ror:4 row_mask:0xf bank_mask:0xf bound_ctrl:1
	v_mov_b32_e32 v147, 1.0
	v_mov_b32_e32 v148, 0
	v_add_f32_dpp v133, v133, v133 quad_perm:[2,3,0,1] row_mask:0xf bank_mask:0xf bound_ctrl:1
	v_mov_b32_e32 v149, 0
	s_nop 0
	v_add_f32_dpp v133, v133, v133 quad_perm:[1,0,3,2] row_mask:0xf bank_mask:0xf bound_ctrl:1
	ds_write_b32 v134, v133
	v_fma_f32 v133, v86, v86, 0
	v_fmac_f32_e32 v133, v82, v82
	v_fmac_f32_e32 v133, v90, v90
	v_fmac_f32_e32 v133, v94, v94
	v_lshl_add_u32 v134, v178, 4, v132
	s_nop 0
	v_add_f32_dpp v133, v133, v133 row_ror:8 row_mask:0xf bank_mask:0xf bound_ctrl:1
	s_nop 1
	v_add_f32_dpp v133, v133, v133 row_ror:4 row_mask:0xf bank_mask:0xf bound_ctrl:1
	s_nop 1
	v_add_f32_dpp v133, v133, v133 quad_perm:[2,3,0,1] row_mask:0xf bank_mask:0xf bound_ctrl:1
	s_nop 1
	v_add_f32_dpp v133, v133, v133 quad_perm:[1,0,3,2] row_mask:0xf bank_mask:0xf bound_ctrl:1
	ds_write_b32 v134, v133
	v_fma_f32 v133, v87, v87, 0
	v_fmac_f32_e32 v133, v83, v83
	v_fmac_f32_e32 v133, v91, v91
	v_fmac_f32_e32 v133, v95, v95
	v_lshl_add_u32 v134, v181, 4, v132
	s_nop 0
	v_add_f32_dpp v133, v133, v133 row_ror:8 row_mask:0xf bank_mask:0xf bound_ctrl:1
	s_nop 1
	v_add_f32_dpp v133, v133, v133 row_ror:4 row_mask:0xf bank_mask:0xf bound_ctrl:1
	s_nop 1
	v_add_f32_dpp v133, v133, v133 quad_perm:[2,3,0,1] row_mask:0xf bank_mask:0xf bound_ctrl:1
	s_nop 1
	v_add_f32_dpp v133, v133, v133 quad_perm:[1,0,3,2] row_mask:0xf bank_mask:0xf bound_ctrl:1
	ds_write_b32 v134, v133
	v_fma_f32 v133, v88, v88, 0
	v_fmac_f32_e32 v133, v84, v84
	v_fmac_f32_e32 v133, v92, v92
	v_fmac_f32_e32 v133, v96, v96
	v_lshl_add_u32 v134, v180, 4, v132
	s_nop 0
	v_add_f32_dpp v133, v133, v133 row_ror:8 row_mask:0xf bank_mask:0xf bound_ctrl:1
	s_nop 1
	v_add_f32_dpp v133, v133, v133 row_ror:4 row_mask:0xf bank_mask:0xf bound_ctrl:1
	s_nop 1
	v_add_f32_dpp v133, v133, v133 quad_perm:[2,3,0,1] row_mask:0xf bank_mask:0xf bound_ctrl:1
	s_nop 1
	v_add_f32_dpp v133, v133, v133 quad_perm:[1,0,3,2] row_mask:0xf bank_mask:0xf bound_ctrl:1
	ds_write_b32 v134, v133
	v_fma_f32 v133, v89, v89, 0
	v_fmac_f32_e32 v133, v85, v85
	v_fmac_f32_e32 v133, v93, v93
	v_fmac_f32_e32 v133, v97, v97
	v_lshl_add_u32 v134, v179, 4, v132
	s_nop 0
	v_add_f32_dpp v133, v133, v133 row_ror:8 row_mask:0xf bank_mask:0xf bound_ctrl:1
	s_nop 1
	v_add_f32_dpp v133, v133, v133 row_ror:4 row_mask:0xf bank_mask:0xf bound_ctrl:1
	s_nop 1
	v_add_f32_dpp v133, v133, v133 quad_perm:[2,3,0,1] row_mask:0xf bank_mask:0xf bound_ctrl:1
	s_nop 1
	v_add_f32_dpp v133, v133, v133 quad_perm:[1,0,3,2] row_mask:0xf bank_mask:0xf bound_ctrl:1
	ds_write_b32 v134, v133
	v_fma_f32 v133, v70, v70, 0
	v_fmac_f32_e32 v133, v66, v66
	v_fmac_f32_e32 v133, v74, v74
	v_fmac_f32_e32 v133, v78, v78
	v_lshl_add_u32 v134, v174, 4, v132
	s_nop 0
	v_add_f32_dpp v133, v133, v133 row_ror:8 row_mask:0xf bank_mask:0xf bound_ctrl:1
	s_nop 1
	v_add_f32_dpp v133, v133, v133 row_ror:4 row_mask:0xf bank_mask:0xf bound_ctrl:1
	s_nop 1
	v_add_f32_dpp v133, v133, v133 quad_perm:[2,3,0,1] row_mask:0xf bank_mask:0xf bound_ctrl:1
	s_nop 1
	v_add_f32_dpp v133, v133, v133 quad_perm:[1,0,3,2] row_mask:0xf bank_mask:0xf bound_ctrl:1
	ds_write_b32 v134, v133
	v_fma_f32 v133, v71, v71, 0
	v_fmac_f32_e32 v133, v67, v67
	v_fmac_f32_e32 v133, v75, v75
	v_fmac_f32_e32 v133, v79, v79
	v_lshl_add_u32 v134, v177, 4, v132
	s_nop 0
	v_add_f32_dpp v133, v133, v133 row_ror:8 row_mask:0xf bank_mask:0xf bound_ctrl:1
	s_nop 1
	v_add_f32_dpp v133, v133, v133 row_ror:4 row_mask:0xf bank_mask:0xf bound_ctrl:1
	s_nop 1
	v_add_f32_dpp v133, v133, v133 quad_perm:[2,3,0,1] row_mask:0xf bank_mask:0xf bound_ctrl:1
	s_nop 1
	v_add_f32_dpp v133, v133, v133 quad_perm:[1,0,3,2] row_mask:0xf bank_mask:0xf bound_ctrl:1
	ds_write_b32 v134, v133
	v_fma_f32 v133, v72, v72, 0
	v_fmac_f32_e32 v133, v68, v68
	v_fmac_f32_e32 v133, v76, v76
	v_fmac_f32_e32 v133, v80, v80
	v_lshl_add_u32 v134, v176, 4, v132
	s_nop 0
	v_add_f32_dpp v133, v133, v133 row_ror:8 row_mask:0xf bank_mask:0xf bound_ctrl:1
	s_nop 1
	v_add_f32_dpp v133, v133, v133 row_ror:4 row_mask:0xf bank_mask:0xf bound_ctrl:1
	s_nop 1
	v_add_f32_dpp v133, v133, v133 quad_perm:[2,3,0,1] row_mask:0xf bank_mask:0xf bound_ctrl:1
	s_nop 1
	v_add_f32_dpp v133, v133, v133 quad_perm:[1,0,3,2] row_mask:0xf bank_mask:0xf bound_ctrl:1
	ds_write_b32 v134, v133
	v_fma_f32 v133, v73, v73, 0
	v_fmac_f32_e32 v133, v69, v69
	v_fmac_f32_e32 v133, v77, v77
	v_fmac_f32_e32 v133, v81, v81
	v_lshl_add_u32 v134, v175, 4, v132
	s_nop 0
	v_add_f32_dpp v133, v133, v133 row_ror:8 row_mask:0xf bank_mask:0xf bound_ctrl:1
	s_nop 1
	v_add_f32_dpp v133, v133, v133 row_ror:4 row_mask:0xf bank_mask:0xf bound_ctrl:1
	s_nop 1
	v_add_f32_dpp v133, v133, v133 quad_perm:[2,3,0,1] row_mask:0xf bank_mask:0xf bound_ctrl:1
	s_nop 1
	v_add_f32_dpp v133, v133, v133 quad_perm:[1,0,3,2] row_mask:0xf bank_mask:0xf bound_ctrl:1
	ds_write_b32 v134, v133
	v_fma_f32 v133, v54, v54, 0
	v_fmac_f32_e32 v133, v50, v50
	v_fmac_f32_e32 v133, v58, v58
	v_fmac_f32_e32 v133, v62, v62
	v_lshl_add_u32 v134, v173, 4, v132
	s_nop 0
	v_add_f32_dpp v133, v133, v133 row_ror:8 row_mask:0xf bank_mask:0xf bound_ctrl:1
	s_nop 1
	v_add_f32_dpp v133, v133, v133 row_ror:4 row_mask:0xf bank_mask:0xf bound_ctrl:1
	s_nop 1
	v_add_f32_dpp v133, v133, v133 quad_perm:[2,3,0,1] row_mask:0xf bank_mask:0xf bound_ctrl:1
	s_nop 1
	v_add_f32_dpp v133, v133, v133 quad_perm:[1,0,3,2] row_mask:0xf bank_mask:0xf bound_ctrl:1
	ds_write_b32 v134, v133
	v_fma_f32 v133, v55, v55, 0
	v_fmac_f32_e32 v133, v51, v51
	v_fmac_f32_e32 v133, v59, v59
	v_fmac_f32_e32 v133, v63, v63
	v_lshl_add_u32 v134, v172, 4, v132
	s_nop 0
	v_add_f32_dpp v133, v133, v133 row_ror:8 row_mask:0xf bank_mask:0xf bound_ctrl:1
	s_nop 1
	v_add_f32_dpp v133, v133, v133 row_ror:4 row_mask:0xf bank_mask:0xf bound_ctrl:1
	s_nop 1
	v_add_f32_dpp v133, v133, v133 quad_perm:[2,3,0,1] row_mask:0xf bank_mask:0xf bound_ctrl:1
	s_nop 1
	v_add_f32_dpp v133, v133, v133 quad_perm:[1,0,3,2] row_mask:0xf bank_mask:0xf bound_ctrl:1
	ds_write_b32 v134, v133
	v_fma_f32 v133, v56, v56, 0
	v_fmac_f32_e32 v133, v52, v52
	v_fmac_f32_e32 v133, v60, v60
	v_fmac_f32_e32 v133, v64, v64
	v_lshl_add_u32 v134, v171, 4, v132
	s_nop 0
	v_add_f32_dpp v133, v133, v133 row_ror:8 row_mask:0xf bank_mask:0xf bound_ctrl:1
	s_nop 1
	v_add_f32_dpp v133, v133, v133 row_ror:4 row_mask:0xf bank_mask:0xf bound_ctrl:1
	s_nop 1
	v_add_f32_dpp v133, v133, v133 quad_perm:[2,3,0,1] row_mask:0xf bank_mask:0xf bound_ctrl:1
	s_nop 1
	v_add_f32_dpp v133, v133, v133 quad_perm:[1,0,3,2] row_mask:0xf bank_mask:0xf bound_ctrl:1
	ds_write_b32 v134, v133
	v_fma_f32 v133, v57, v57, 0
	v_fmac_f32_e32 v133, v53, v53
	v_fmac_f32_e32 v133, v61, v61
	v_fmac_f32_e32 v133, v65, v65
	v_lshl_add_u32 v134, v170, 4, v132
	s_nop 0
	v_add_f32_dpp v133, v133, v133 row_ror:8 row_mask:0xf bank_mask:0xf bound_ctrl:1
	s_nop 1
	v_add_f32_dpp v133, v133, v133 row_ror:4 row_mask:0xf bank_mask:0xf bound_ctrl:1
	s_nop 1
	v_add_f32_dpp v133, v133, v133 quad_perm:[2,3,0,1] row_mask:0xf bank_mask:0xf bound_ctrl:1
	s_nop 1
	v_add_f32_dpp v133, v133, v133 quad_perm:[1,0,3,2] row_mask:0xf bank_mask:0xf bound_ctrl:1
	ds_write_b32 v134, v133
	v_fma_f32 v133, v38, v38, 0
	v_fmac_f32_e32 v133, v34, v34
	v_fmac_f32_e32 v133, v42, v42
	v_fmac_f32_e32 v133, v46, v46
	v_lshl_add_u32 v134, v166, 4, v132
	s_nop 0
	v_add_f32_dpp v133, v133, v133 row_ror:8 row_mask:0xf bank_mask:0xf bound_ctrl:1
	s_nop 1
	v_add_f32_dpp v133, v133, v133 row_ror:4 row_mask:0xf bank_mask:0xf bound_ctrl:1
	s_nop 1
	v_add_f32_dpp v133, v133, v133 quad_perm:[2,3,0,1] row_mask:0xf bank_mask:0xf bound_ctrl:1
	s_nop 1
	v_add_f32_dpp v133, v133, v133 quad_perm:[1,0,3,2] row_mask:0xf bank_mask:0xf bound_ctrl:1
	ds_write_b32 v134, v133
	v_fma_f32 v133, v39, v39, 0
	v_fmac_f32_e32 v133, v35, v35
	v_fmac_f32_e32 v133, v43, v43
	v_fmac_f32_e32 v133, v47, v47
	v_lshl_add_u32 v134, v169, 4, v132
	s_nop 0
	v_add_f32_dpp v133, v133, v133 row_ror:8 row_mask:0xf bank_mask:0xf bound_ctrl:1
	s_nop 1
	v_add_f32_dpp v133, v133, v133 row_ror:4 row_mask:0xf bank_mask:0xf bound_ctrl:1
	s_nop 1
	v_add_f32_dpp v133, v133, v133 quad_perm:[2,3,0,1] row_mask:0xf bank_mask:0xf bound_ctrl:1
	s_nop 1
	v_add_f32_dpp v133, v133, v133 quad_perm:[1,0,3,2] row_mask:0xf bank_mask:0xf bound_ctrl:1
	ds_write_b32 v134, v133
	v_fma_f32 v133, v40, v40, 0
	v_fmac_f32_e32 v133, v36, v36
	v_fmac_f32_e32 v133, v44, v44
	v_fmac_f32_e32 v133, v48, v48
	v_lshl_add_u32 v134, v168, 4, v132
	s_nop 0
	v_add_f32_dpp v133, v133, v133 row_ror:8 row_mask:0xf bank_mask:0xf bound_ctrl:1
	s_nop 1
	v_add_f32_dpp v133, v133, v133 row_ror:4 row_mask:0xf bank_mask:0xf bound_ctrl:1
	s_nop 1
	v_add_f32_dpp v133, v133, v133 quad_perm:[2,3,0,1] row_mask:0xf bank_mask:0xf bound_ctrl:1
	s_nop 1
	v_add_f32_dpp v133, v133, v133 quad_perm:[1,0,3,2] row_mask:0xf bank_mask:0xf bound_ctrl:1
	ds_write_b32 v134, v133
	v_fma_f32 v133, v41, v41, 0
	v_fmac_f32_e32 v133, v37, v37
	v_fmac_f32_e32 v133, v45, v45
	v_fmac_f32_e32 v133, v49, v49
	v_lshl_add_u32 v134, v167, 4, v132
	s_nop 0
	v_add_f32_dpp v133, v133, v133 row_ror:8 row_mask:0xf bank_mask:0xf bound_ctrl:1
	s_nop 1
	v_add_f32_dpp v133, v133, v133 row_ror:4 row_mask:0xf bank_mask:0xf bound_ctrl:1
	s_nop 1
	v_add_f32_dpp v133, v133, v133 quad_perm:[2,3,0,1] row_mask:0xf bank_mask:0xf bound_ctrl:1
	s_nop 1
	v_add_f32_dpp v133, v133, v133 quad_perm:[1,0,3,2] row_mask:0xf bank_mask:0xf bound_ctrl:1
	ds_write_b32 v134, v133
	v_fma_f32 v133, v22, v22, 0
	v_fmac_f32_e32 v133, v18, v18
	v_fmac_f32_e32 v133, v26, v26
	v_fmac_f32_e32 v133, v30, v30
	v_lshl_add_u32 v134, v160, 4, v132
	s_nop 0
	v_add_f32_dpp v133, v133, v133 row_ror:8 row_mask:0xf bank_mask:0xf bound_ctrl:1
	s_nop 1
	v_add_f32_dpp v133, v133, v133 row_ror:4 row_mask:0xf bank_mask:0xf bound_ctrl:1
	s_nop 1
	v_add_f32_dpp v133, v133, v133 quad_perm:[2,3,0,1] row_mask:0xf bank_mask:0xf bound_ctrl:1
	s_nop 1
	v_add_f32_dpp v133, v133, v133 quad_perm:[1,0,3,2] row_mask:0xf bank_mask:0xf bound_ctrl:1
	ds_write_b32 v134, v133
	v_fma_f32 v133, v23, v23, 0
	v_fmac_f32_e32 v133, v19, v19
	v_fmac_f32_e32 v133, v27, v27
	v_fmac_f32_e32 v133, v31, v31
	v_lshl_add_u32 v134, v165, 4, v132
	s_nop 0
	v_add_f32_dpp v133, v133, v133 row_ror:8 row_mask:0xf bank_mask:0xf bound_ctrl:1
	s_nop 1
	v_add_f32_dpp v133, v133, v133 row_ror:4 row_mask:0xf bank_mask:0xf bound_ctrl:1
	s_nop 1
	v_add_f32_dpp v133, v133, v133 quad_perm:[2,3,0,1] row_mask:0xf bank_mask:0xf bound_ctrl:1
	s_nop 1
	v_add_f32_dpp v133, v133, v133 quad_perm:[1,0,3,2] row_mask:0xf bank_mask:0xf bound_ctrl:1
	ds_write_b32 v134, v133
	v_fma_f32 v133, v24, v24, 0
	v_fmac_f32_e32 v133, v20, v20
	v_fmac_f32_e32 v133, v28, v28
	v_fmac_f32_e32 v133, v32, v32
	v_lshl_add_u32 v134, v164, 4, v132
	s_nop 0
	v_add_f32_dpp v133, v133, v133 row_ror:8 row_mask:0xf bank_mask:0xf bound_ctrl:1
	s_nop 1
	v_add_f32_dpp v133, v133, v133 row_ror:4 row_mask:0xf bank_mask:0xf bound_ctrl:1
	s_nop 1
	v_add_f32_dpp v133, v133, v133 quad_perm:[2,3,0,1] row_mask:0xf bank_mask:0xf bound_ctrl:1
	s_nop 1
	v_add_f32_dpp v133, v133, v133 quad_perm:[1,0,3,2] row_mask:0xf bank_mask:0xf bound_ctrl:1
	ds_write_b32 v134, v133
	v_fma_f32 v133, v25, v25, 0
	v_fmac_f32_e32 v133, v21, v21
	v_fmac_f32_e32 v133, v29, v29
	v_fmac_f32_e32 v133, v33, v33
	v_lshl_add_u32 v134, v163, 4, v132
	s_nop 0
	v_add_f32_dpp v133, v133, v133 row_ror:8 row_mask:0xf bank_mask:0xf bound_ctrl:1
	s_nop 1
	v_add_f32_dpp v133, v133, v133 row_ror:4 row_mask:0xf bank_mask:0xf bound_ctrl:1
	s_nop 1
	v_add_f32_dpp v133, v133, v133 quad_perm:[2,3,0,1] row_mask:0xf bank_mask:0xf bound_ctrl:1
	s_nop 1
	v_add_f32_dpp v133, v133, v133 quad_perm:[1,0,3,2] row_mask:0xf bank_mask:0xf bound_ctrl:1
	ds_write_b32 v134, v133
	v_fma_f32 v133, v6, v6, 0
	v_fmac_f32_e32 v133, v2, v2
	v_fmac_f32_e32 v133, v10, v10
	v_fmac_f32_e32 v133, v14, v14
	v_lshl_add_u32 v134, v153, 4, v132
	s_nop 0
	v_add_f32_dpp v133, v133, v133 row_ror:8 row_mask:0xf bank_mask:0xf bound_ctrl:1
	s_nop 1
	v_add_f32_dpp v133, v133, v133 row_ror:4 row_mask:0xf bank_mask:0xf bound_ctrl:1
	s_nop 1
	v_add_f32_dpp v133, v133, v133 quad_perm:[2,3,0,1] row_mask:0xf bank_mask:0xf bound_ctrl:1
	s_nop 1
	v_add_f32_dpp v133, v133, v133 quad_perm:[1,0,3,2] row_mask:0xf bank_mask:0xf bound_ctrl:1
	ds_write_b32 v134, v133
	v_fma_f32 v133, v7, v7, 0
	v_fmac_f32_e32 v133, v3, v3
	v_fmac_f32_e32 v133, v11, v11
	v_fmac_f32_e32 v133, v15, v15
	v_lshl_add_u32 v134, v159, 4, v132
	s_nop 0
	v_add_f32_dpp v133, v133, v133 row_ror:8 row_mask:0xf bank_mask:0xf bound_ctrl:1
	s_nop 1
	v_add_f32_dpp v133, v133, v133 row_ror:4 row_mask:0xf bank_mask:0xf bound_ctrl:1
	s_nop 1
	v_add_f32_dpp v133, v133, v133 quad_perm:[2,3,0,1] row_mask:0xf bank_mask:0xf bound_ctrl:1
	s_nop 1
	v_add_f32_dpp v133, v133, v133 quad_perm:[1,0,3,2] row_mask:0xf bank_mask:0xf bound_ctrl:1
	ds_write_b32 v134, v133
	v_fma_f32 v133, v8, v8, 0
	v_fmac_f32_e32 v133, v4, v4
	v_fmac_f32_e32 v133, v12, v12
	v_fmac_f32_e32 v133, v16, v16
	v_lshl_add_u32 v134, v157, 4, v132
	v_lshl_add_u32 v132, v156, 4, v132
	v_add_f32_dpp v133, v133, v133 row_ror:8 row_mask:0xf bank_mask:0xf bound_ctrl:1
	s_nop 1
	v_add_f32_dpp v133, v133, v133 row_ror:4 row_mask:0xf bank_mask:0xf bound_ctrl:1
	s_nop 1
	v_add_f32_dpp v133, v133, v133 quad_perm:[2,3,0,1] row_mask:0xf bank_mask:0xf bound_ctrl:1
	s_nop 1
	v_add_f32_dpp v133, v133, v133 quad_perm:[1,0,3,2] row_mask:0xf bank_mask:0xf bound_ctrl:1
	ds_write_b32 v134, v133
	v_fma_f32 v133, v9, v9, 0
	v_fmac_f32_e32 v133, v5, v5
	v_fmac_f32_e32 v133, v13, v13
	v_fmac_f32_e32 v133, v17, v17
	v_mov_b32_e32 v134, 0
	s_nop 0
	v_add_f32_dpp v133, v133, v133 row_ror:8 row_mask:0xf bank_mask:0xf bound_ctrl:1
	s_nop 1
	v_add_f32_dpp v133, v133, v133 row_ror:4 row_mask:0xf bank_mask:0xf bound_ctrl:1
	s_nop 1
	v_add_f32_dpp v133, v133, v133 quad_perm:[2,3,0,1] row_mask:0xf bank_mask:0xf bound_ctrl:1
	s_nop 1
	v_add_f32_dpp v133, v133, v133 quad_perm:[1,0,3,2] row_mask:0xf bank_mask:0xf bound_ctrl:1
	ds_write_b32 v132, v133
	v_mov_b32_e32 v132, 1.0
	v_mov_b32_e32 v133, 1.0
	s_and_saveexec_b64 s[0:1], vcc
	s_cbranch_execz .LBB2_24
	v_mov_b32_e32 v133, 0
	v_or_b32_e32 v132, s2, v187
	v_lshlrev_b32_e32 v140, 3, v130
	v_mov_b32_e32 v141, v133
	v_lshlrev_b32_e32 v132, 7, v132
	v_lshl_add_u64 v[146:147], s[16:17], 0, v[140:141]
	s_movk_i32 s4, 0x4000
	v_lshl_add_u64 v[134:135], s[16:17], 0, v[132:133]
	v_lshl_add_u64 v[132:133], s[18:19], 0, v[132:133]
	v_add_co_u32_e32 v146, vcc, s4, v146
	v_lshl_add_u64 v[134:135], v[134:135], 0, v[140:141]
	v_lshl_add_u64 v[132:133], v[132:133], 0, v[140:141]
	v_lshl_add_u64 v[148:149], s[18:19], 0, v[140:141]
	v_addc_co_u32_e32 v147, vcc, 0, v147, vcc
	global_load_dwordx2 v[142:143], v[134:135], off
	global_load_dwordx2 v[144:145], v[132:133], off
	s_nop 0
	global_load_dwordx2 v[132:133], v140, s[16:17] offset:128
	global_load_dwordx2 v[134:135], v140, s[18:19] offset:128
	global_load_dwordx2 v[138:139], v140, s[16:17] offset:2048
	s_nop 0
	global_load_dwordx2 v[140:141], v140, s[18:19] offset:2048
	v_add_co_u32_e32 v148, vcc, s4, v148
	global_load_dwordx2 v[146:147], v[146:147], off
	s_nop 0
	v_addc_co_u32_e32 v149, vcc, 0, v149, vcc
	global_load_dwordx2 v[148:149], v[148:149], off
.LBB2_24:
	s_or_b64 exec, exec, s[0:1]
	s_and_b32 s4, s20, 0x700000
	s_cmp_lt_u32 s3, 64
	s_cselect_b64 vcc, -1, 0
	s_and_b64 s[0:1], vcc, exec
	s_cselect_b32 s1, s13, s15
	s_cselect_b32 s0, s12, s14
	s_lshl_b32 s3, s4, 1
	v_mov_b32_e32 v137, 0x3e0293ee
	s_add_u32 s0, s0, s3
	v_cndmask_b32_e32 v158, 1.0, v137, vcc
	s_addc_u32 s1, s1, 0
	v_lshlrev_b32_e32 v136, 6, v136
	v_lshlrev_b32_e32 v137, 2, v130
	v_lshlrev_b32_e32 v130, 4, v130
	v_add3_u32 v162, 0, v136, v137
	v_add_u32_e32 v182, 0, v130
	v_lshl_add_u64 v[136:137], s[0:1], 0, v[130:131]
	v_lshrrev_b16_e32 v130, 2, v0
	v_lshlrev_b16_e32 v192, 6, v154
	v_and_b32_e32 v191, 12, v130
	v_bitop3_b16 v194, v192, v130, 12 bitop3:0xf8
	v_lshlrev_b32_e32 v130, 2, v187
	v_lshlrev_b32_e32 v189, 2, v189
	v_lshlrev_b32_e32 v188, 2, v188
	v_or_b32_e32 v154, v130, v1
	v_bitop3_b32 v130, v130, 1, v1 bitop3:0x36
	v_lshlrev_b32_e32 v190, 2, v190
	v_or_b32_e32 v195, v189, v1
	v_or_b32_e32 v196, v188, v1
	v_lshl_add_u32 v154, v154, 2, 0
	v_lshl_add_u32 v130, v130, 2, 0
	v_or_b32_e32 v193, v190, v1
	v_bitop3_b32 v190, v190, 1, v1 bitop3:0x36
	v_lshl_add_u32 v195, v195, 2, 0
	v_bitop3_b32 v189, v189, 1, v1 bitop3:0x36
	v_lshl_add_u32 v196, v196, 2, 0
	v_bitop3_b32 v188, v188, 1, v1 bitop3:0x36
	s_waitcnt lgkmcnt(0)
	s_barrier
	v_lshl_add_u32 v193, v193, 2, 0
	v_lshl_add_u32 v190, v190, 2, 0
	v_lshl_add_u32 v189, v189, 2, 0
	v_lshl_add_u32 v188, v188, 2, 0
	ds_read_b32 v154, v154
	ds_read_b32 v130, v130
	ds_read_b32 v197, v193
	ds_read_b32 v198, v190
	ds_read_b32 v195, v195
	ds_read_b32 v199, v189
	ds_read_b32 v196, v196
	ds_read_b32 v200, v188
	s_waitcnt lgkmcnt(6)
	v_add_f32_e32 v130, v154, v130
	v_bfrev_b32_e32 v154, 44
	v_fmamk_f32 v130, v130, 0x3c000000, v154
	v_rsq_f32_e32 v188, v130
	v_bitop3_b16 v201, v192, 16, v191 bitop3:0xfe
	v_bitop3_b16 v202, v192, 32, v191 bitop3:0xfe
	v_bitop3_b16 v130, v192, 48, v191 bitop3:0xfe
	v_mul_f32_e32 v188, v158, v188
	v_mov_b32_e32 v190, v118
	v_mov_b32_e32 v191, v114
	v_mov_b32_e32 v192, v122
	v_mov_b32_e32 v193, v126
	v_pk_mul_f32 v[190:191], v[190:191], v[188:189] op_sel_hi:[1,0]
	v_pk_mul_f32 v[188:189], v[192:193], v[188:189] op_sel_hi:[1,0]
	v_and_b32_e32 v161, 0x80, v0
	s_movk_i32 s1, 0x4c
	s_waitcnt vmcnt(6)
	v_pk_mul_f32 v[192:193], v[144:145], v[188:189]
	s_movk_i32 s0, 0x110
	v_and_or_b32 v187, v187, s1, v161
	v_pk_fma_f32 v[192:193], v[142:143], v[190:191], v[192:193]
	v_pk_mul_f32 v[190:191], v[144:145], v[190:191]
	v_mad_u32_u24 v187, v187, s0, v162
	v_pk_fma_f32 v[188:189], v[142:143], v[188:189], v[190:191] neg_lo:[0,0,1] neg_hi:[0,0,1]
	v_cvt_pk_f16_f32 v114, v192, v193
	v_cvt_pk_f16_f32 v122, v188, v189
	v_add_u32_e32 v118, 0x1000, v187
	ds_write2_b32 v118, v114, v122 offset1:32
	s_waitcnt lgkmcnt(5)
	v_add_f32_e32 v114, v197, v198
	v_fmamk_f32 v114, v114, 0x3c000000, v154
	v_rsq_f32_e32 v114, v114
	s_waitcnt vmcnt(4)
	v_pk_mul_f32 v[190:191], v[142:143], v[134:135]
	v_mov_b32_e32 v126, v123
	v_pk_mul_f32 v[188:189], v[144:145], v[134:135]
	v_mul_f32_e32 v122, v158, v114
	v_or_b32_sdwa v114, v161, v194 dst_sel:DWORD dst_unused:UNUSED_PAD src0_sel:DWORD src1_sel:WORD_0
	v_mad_u32_u24 v187, v114, s0, v162
	v_mov_b32_e32 v114, v119
	v_pk_fma_f32 v[190:191], v[144:145], v[132:133], v[190:191]
	v_pk_mul_f32 v[114:115], v[114:115], v[122:123] op_sel_hi:[1,0]
	v_pk_mul_f32 v[122:123], v[126:127], v[122:123] op_sel_hi:[1,0]
	v_pk_fma_f32 v[188:189], v[142:143], v[132:133], v[188:189] neg_lo:[0,0,1] neg_hi:[0,0,1]
	v_pk_mul_f32 v[126:127], v[190:191], v[122:123]
	v_mov_b32_e32 v192, v124
	v_pk_fma_f32 v[126:127], v[188:189], v[114:115], v[126:127]
	v_pk_mul_f32 v[114:115], v[190:191], v[114:115]
	v_cvt_pk_f16_f32 v119, v126, v127
	v_pk_fma_f32 v[114:115], v[188:189], v[122:123], v[114:115] neg_lo:[0,0,1] neg_hi:[0,0,1]
	v_pk_mul_f32 v[122:123], v[134:135], v[190:191]
	v_cvt_pk_f16_f32 v115, v114, v115
	v_add_u32_e32 v114, 0x1000, v187
	ds_write2_b32 v114, v119, v115 offset0:68 offset1:100
	s_waitcnt lgkmcnt(4)
	v_add_f32_e32 v115, v195, v199
	v_fmamk_f32 v115, v115, 0x3c000000, v154
	v_rsq_f32_e32 v115, v115
	v_pk_mul_f32 v[126:127], v[132:133], v[190:191]
	v_pk_fma_f32 v[122:123], v[132:133], v[188:189], v[122:123] neg_lo:[0,0,1] neg_hi:[0,0,1]
	v_pk_fma_f32 v[126:127], v[134:135], v[188:189], v[126:127]
	v_mul_f32_e32 v188, v158, v115
	v_mov_b32_e32 v190, v120
	v_mov_b32_e32 v191, v116
	v_mov_b32_e32 v193, v128
	v_pk_mul_f32 v[190:191], v[190:191], v[188:189] op_sel_hi:[1,0]
	v_pk_mul_f32 v[188:189], v[192:193], v[188:189] op_sel_hi:[1,0]
	v_mov_b32_e32 v128, v125
	v_pk_mul_f32 v[192:193], v[126:127], v[188:189]
	s_movk_i32 s1, 0x5c
	v_pk_fma_f32 v[192:193], v[122:123], v[190:191], v[192:193]
	v_pk_mul_f32 v[190:191], v[126:127], v[190:191]
	v_cvt_pk_f16_f32 v115, v192, v193
	v_pk_fma_f32 v[188:189], v[122:123], v[188:189], v[190:191] neg_lo:[0,0,1] neg_hi:[0,0,1]
	s_movk_i32 s3, 0x6c
	v_cvt_pk_f16_f32 v116, v188, v189
	ds_write2_b32 v114, v115, v116 offset0:136 offset1:168
	s_waitcnt lgkmcnt(3)
	v_add_f32_e32 v115, v196, v200
	v_fmamk_f32 v115, v115, 0x3c000000, v154
	v_rsq_f32_e32 v115, v115
	v_pk_mul_f32 v[188:189], v[134:135], v[126:127]
	v_pk_mul_f32 v[126:127], v[132:133], v[126:127]
	v_mov_b32_e32 v116, v121
	v_mul_f32_e32 v120, v158, v115
	v_pk_fma_f32 v[188:189], v[132:133], v[122:123], v[188:189] neg_lo:[0,0,1] neg_hi:[0,0,1]
	v_pk_fma_f32 v[122:123], v[134:135], v[122:123], v[126:127]
	v_pk_mul_f32 v[116:117], v[116:117], v[120:121] op_sel_hi:[1,0]
	v_pk_mul_f32 v[120:121], v[128:129], v[120:121] op_sel_hi:[1,0]
	v_mov_b32_e32 v126, v106
	v_pk_mul_f32 v[124:125], v[122:123], v[120:121]
	v_mov_b32_e32 v127, v110
	v_pk_fma_f32 v[124:125], v[188:189], v[116:117], v[124:125]
	v_pk_mul_f32 v[116:117], v[122:123], v[116:117]
	v_cvt_pk_f16_f32 v115, v124, v125
	v_pk_fma_f32 v[116:117], v[188:189], v[120:121], v[116:117] neg_lo:[0,0,1] neg_hi:[0,0,1]
	v_lshlrev_b32_e32 v120, 2, v186
	v_cvt_pk_f16_f32 v116, v116, v117
	ds_write2_b32 v114, v115, v116 offset0:204 offset1:236
	v_lshlrev_b32_e32 v115, 2, v183
	v_or_b32_e32 v119, v115, v1
	v_bitop3_b32 v115, v115, 1, v1 bitop3:0x36
	v_lshlrev_b32_e32 v122, 2, v185
	v_lshlrev_b32_e32 v124, 2, v184
	v_lshl_add_u32 v119, v119, 2, 0
	v_lshl_add_u32 v115, v115, 2, 0
	v_or_b32_e32 v121, v120, v1
	v_bitop3_b32 v120, v120, 1, v1 bitop3:0x36
	v_or_b32_e32 v123, v122, v1
	v_bitop3_b32 v122, v122, 1, v1 bitop3:0x36
	v_or_b32_e32 v125, v124, v1
	v_bitop3_b32 v124, v124, 1, v1 bitop3:0x36
	v_lshl_add_u32 v121, v121, 2, 0
	v_lshl_add_u32 v120, v120, 2, 0
	v_lshl_add_u32 v123, v123, 2, 0
	v_lshl_add_u32 v122, v122, 2, 0
	v_lshl_add_u32 v125, v125, 2, 0
	v_lshl_add_u32 v124, v124, 2, 0
	ds_read_b32 v119, v119
	ds_read_b32 v115, v115
	ds_read_b32 v128, v121
	ds_read_b32 v129, v120
	ds_read_b32 v184, v123
	ds_read_b32 v185, v122
	ds_read_b32 v186, v125
	ds_read_b32 v187, v124
	s_waitcnt lgkmcnt(6)
	v_add_f32_e32 v115, v119, v115
	v_fmamk_f32 v115, v115, 0x3c000000, v154
	v_rsq_f32_e32 v115, v115
	s_waitcnt vmcnt(2)
	v_pk_mul_f32 v[120:121], v[142:143], v[140:141]
	v_mov_b32_e32 v124, v102
	v_mov_b32_e32 v125, v98
	v_mul_f32_e32 v122, v158, v115
	v_pk_mul_f32 v[116:117], v[144:145], v[140:141]
	v_pk_fma_f32 v[120:121], v[144:145], v[138:139], v[120:121]
	v_pk_mul_f32 v[124:125], v[124:125], v[122:123] op_sel_hi:[1,0]
	v_pk_mul_f32 v[122:123], v[126:127], v[122:123] op_sel_hi:[1,0]
	v_pk_fma_f32 v[116:117], v[142:143], v[138:139], v[116:117] neg_lo:[0,0,1] neg_hi:[0,0,1]
	v_pk_mul_f32 v[126:127], v[120:121], v[122:123]
	v_and_or_b32 v115, v183, s1, v161
	v_pk_fma_f32 v[126:127], v[116:117], v[124:125], v[126:127]
	v_pk_mul_f32 v[124:125], v[120:121], v[124:125]
	v_mad_u32_u24 v115, v115, s0, v162
	v_pk_fma_f32 v[122:123], v[116:117], v[122:123], v[124:125] neg_lo:[0,0,1] neg_hi:[0,0,1]
	v_cvt_pk_f16_f32 v98, v126, v127
	v_cvt_pk_f16_f32 v102, v122, v123
	v_add_u32_e32 v106, 0x1000, v115
	ds_write2_b32 v106, v98, v102 offset1:32
	s_waitcnt lgkmcnt(5)
	v_add_f32_e32 v98, v128, v129
	v_fmamk_f32 v98, v98, 0x3c000000, v154
	v_rsq_f32_e32 v98, v98
	v_pk_mul_f32 v[124:125], v[132:133], v[120:121]
	v_mov_b32_e32 v110, v107
	v_pk_mul_f32 v[122:123], v[134:135], v[120:121]
	v_mul_f32_e32 v102, v158, v98
	v_or_b32_sdwa v98, v161, v201 dst_sel:DWORD dst_unused:UNUSED_PAD src0_sel:DWORD src1_sel:WORD_0
	v_mad_u32_u24 v115, v98, s0, v162
	v_mov_b32_e32 v98, v103
	v_pk_fma_f32 v[124:125], v[134:135], v[116:117], v[124:125]
	v_pk_mul_f32 v[98:99], v[98:99], v[102:103] op_sel_hi:[1,0]
	v_pk_mul_f32 v[102:103], v[110:111], v[102:103] op_sel_hi:[1,0]
	v_pk_fma_f32 v[122:123], v[132:133], v[116:117], v[122:123] neg_lo:[0,0,1] neg_hi:[0,0,1]
	v_pk_mul_f32 v[106:107], v[124:125], v[102:103]
	s_movk_i32 s4, 0x7c
	v_pk_fma_f32 v[106:107], v[122:123], v[98:99], v[106:107]
	v_pk_mul_f32 v[98:99], v[124:125], v[98:99]
	v_cvt_pk_f16_f32 v106, v106, v107
	v_pk_fma_f32 v[98:99], v[122:123], v[102:103], v[98:99] neg_lo:[0,0,1] neg_hi:[0,0,1]
	v_pk_mul_f32 v[102:103], v[134:135], v[124:125]
	v_cvt_pk_f16_f32 v99, v98, v99
	v_add_u32_e32 v98, 0x1000, v115
	ds_write2_b32 v98, v106, v99 offset0:68 offset1:100
	s_waitcnt lgkmcnt(4)
	v_add_f32_e32 v99, v184, v185
	v_fmamk_f32 v99, v99, 0x3c000000, v154
	v_rsq_f32_e32 v99, v99
	v_pk_mul_f32 v[106:107], v[132:133], v[124:125]
	v_pk_fma_f32 v[102:103], v[132:133], v[122:123], v[102:103] neg_lo:[0,0,1] neg_hi:[0,0,1]
	v_pk_fma_f32 v[106:107], v[134:135], v[122:123], v[106:107]
	v_mul_f32_e32 v110, v158, v99
	v_mov_b32_e32 v122, v104
	v_mov_b32_e32 v123, v100
	v_mov_b32_e32 v124, v108
	v_mov_b32_e32 v125, v112
	v_pk_mul_f32 v[122:123], v[122:123], v[110:111] op_sel_hi:[1,0]
	v_pk_mul_f32 v[110:111], v[124:125], v[110:111] op_sel_hi:[1,0]
	v_mov_b32_e32 v112, v109
	v_pk_mul_f32 v[124:125], v[106:107], v[110:111]
	v_mov_b32_e32 v109, v94
	v_pk_fma_f32 v[124:125], v[102:103], v[122:123], v[124:125]
	v_pk_mul_f32 v[122:123], v[106:107], v[122:123]
	v_cvt_pk_f16_f32 v99, v124, v125
	v_pk_fma_f32 v[110:111], v[102:103], v[110:111], v[122:123] neg_lo:[0,0,1] neg_hi:[0,0,1]
	v_mov_b32_e32 v94, v91
	v_cvt_pk_f16_f32 v100, v110, v111
	ds_write2_b32 v98, v99, v100 offset0:136 offset1:168
	s_waitcnt lgkmcnt(3)
	v_add_f32_e32 v99, v186, v187
	v_fmamk_f32 v99, v99, 0x3c000000, v154
	v_rsq_f32_e32 v99, v99
	v_pk_mul_f32 v[110:111], v[134:135], v[106:107]
	v_pk_mul_f32 v[106:107], v[132:133], v[106:107]
	v_mov_b32_e32 v100, v105
	v_mul_f32_e32 v104, v158, v99
	v_pk_fma_f32 v[110:111], v[132:133], v[102:103], v[110:111] neg_lo:[0,0,1] neg_hi:[0,0,1]
	v_pk_fma_f32 v[102:103], v[134:135], v[102:103], v[106:107]
	v_pk_mul_f32 v[100:101], v[100:101], v[104:105] op_sel_hi:[1,0]
	v_pk_mul_f32 v[104:105], v[112:113], v[104:105] op_sel_hi:[1,0]
	v_mad_u32_u24 v155, v152, s0, v182
	v_pk_mul_f32 v[106:107], v[102:103], v[104:105]
	s_or_b32 s5, s2, 0x1000
	v_pk_fma_f32 v[106:107], v[110:111], v[100:101], v[106:107]
	v_pk_mul_f32 v[100:101], v[102:103], v[100:101]
	v_cvt_pk_f16_f32 v99, v106, v107
	v_pk_fma_f32 v[100:101], v[110:111], v[104:105], v[100:101] neg_lo:[0,0,1] neg_hi:[0,0,1]
	v_lshlrev_b32_e32 v103, 2, v181
	v_cvt_pk_f16_f32 v100, v100, v101
	ds_write2_b32 v98, v99, v100 offset0:204 offset1:236
	v_lshlrev_b32_e32 v99, 2, v178
	v_or_b32_e32 v102, v99, v1
	v_bitop3_b32 v99, v99, 1, v1 bitop3:0x36
	v_lshlrev_b32_e32 v105, 2, v180
	v_lshlrev_b32_e32 v107, 2, v179
	v_lshl_add_u32 v102, v102, 2, 0
	v_lshl_add_u32 v99, v99, 2, 0
	v_or_b32_e32 v104, v103, v1
	v_bitop3_b32 v103, v103, 1, v1 bitop3:0x36
	v_or_b32_e32 v106, v105, v1
	v_bitop3_b32 v105, v105, 1, v1 bitop3:0x36
	v_or_b32_e32 v108, v107, v1
	v_bitop3_b32 v107, v107, 1, v1 bitop3:0x36
	v_lshl_add_u32 v104, v104, 2, 0
	v_lshl_add_u32 v103, v103, 2, 0
	v_lshl_add_u32 v106, v106, 2, 0
	v_lshl_add_u32 v105, v105, 2, 0
	v_lshl_add_u32 v108, v108, 2, 0
	v_lshl_add_u32 v107, v107, 2, 0
	ds_read_b32 v102, v102
	ds_read_b32 v99, v99
	ds_read_b32 v110, v104
	ds_read_b32 v111, v103
	ds_read_b32 v112, v106
	ds_read_b32 v113, v105
	ds_read_b32 v115, v108
	ds_read_b32 v119, v107
	s_waitcnt lgkmcnt(6)
	v_add_f32_e32 v99, v102, v99
	v_fmamk_f32 v99, v99, 0x3c000000, v154
	v_rsq_f32_e32 v99, v99
	v_pk_mul_f32 v[102:103], v[138:139], v[120:121]
	v_mov_b32_e32 v106, v86
	v_mov_b32_e32 v107, v82
	v_mul_f32_e32 v104, v158, v99
	v_mov_b32_e32 v108, v90
	v_pk_mul_f32 v[100:101], v[140:141], v[120:121]
	v_pk_fma_f32 v[102:103], v[140:141], v[116:117], v[102:103]
	v_pk_mul_f32 v[106:107], v[106:107], v[104:105] op_sel_hi:[1,0]
	v_pk_mul_f32 v[104:105], v[108:109], v[104:105] op_sel_hi:[1,0]
	v_pk_fma_f32 v[100:101], v[138:139], v[116:117], v[100:101] neg_lo:[0,0,1] neg_hi:[0,0,1]
	v_pk_mul_f32 v[108:109], v[102:103], v[104:105]
	v_and_or_b32 v99, v178, s3, v161
	v_pk_fma_f32 v[108:109], v[100:101], v[106:107], v[108:109]
	v_pk_mul_f32 v[106:107], v[102:103], v[106:107]
	v_mad_u32_u24 v99, v99, s0, v162
	v_pk_fma_f32 v[104:105], v[100:101], v[104:105], v[106:107] neg_lo:[0,0,1] neg_hi:[0,0,1]
	v_cvt_pk_f16_f32 v82, v108, v109
	v_cvt_pk_f16_f32 v86, v104, v105
	v_add_u32_e32 v90, 0x1000, v99
	ds_write2_b32 v90, v82, v86 offset1:32
	s_waitcnt lgkmcnt(5)
	v_add_f32_e32 v82, v110, v111
	v_fmamk_f32 v82, v82, 0x3c000000, v154
	v_rsq_f32_e32 v82, v82
	v_pk_mul_f32 v[106:107], v[132:133], v[102:103]
	v_pk_mul_f32 v[104:105], v[134:135], v[102:103]
	v_pk_fma_f32 v[106:107], v[134:135], v[100:101], v[106:107]
	v_mul_f32_e32 v86, v158, v82
	v_or_b32_sdwa v82, v161, v202 dst_sel:DWORD dst_unused:UNUSED_PAD src0_sel:DWORD src1_sel:WORD_0
	v_mad_u32_u24 v99, v82, s0, v162
	v_mov_b32_e32 v82, v87
	v_pk_mul_f32 v[82:83], v[82:83], v[86:87] op_sel_hi:[1,0]
	v_pk_mul_f32 v[86:87], v[94:95], v[86:87] op_sel_hi:[1,0]
	v_pk_fma_f32 v[104:105], v[132:133], v[100:101], v[104:105] neg_lo:[0,0,1] neg_hi:[0,0,1]
	v_pk_mul_f32 v[90:91], v[106:107], v[86:87]
	s_waitcnt vmcnt(0)
	s_cmp_lg_u32 s55, 0
	s_cbranch_scc1 .Lve_touch_done
	s_add_u32 s50, s50, s54
	s_addc_u32 s51, s51, 0
	global_load_dword v254, v252, s[50:51]
	global_load_dword v254, v252, s[50:51] offset:128
.Lve_touch_done:
	v_pk_mul_f32 v[150:151], v[144:145], v[148:149]
	v_pk_fma_f32 v[90:91], v[104:105], v[82:83], v[90:91]
	v_pk_mul_f32 v[82:83], v[106:107], v[82:83]
	v_cvt_pk_f16_f32 v90, v90, v91
	v_pk_fma_f32 v[82:83], v[104:105], v[86:87], v[82:83] neg_lo:[0,0,1] neg_hi:[0,0,1]
	v_pk_mul_f32 v[86:87], v[134:135], v[106:107]
	v_cvt_pk_f16_f32 v83, v82, v83
	v_add_u32_e32 v82, 0x1000, v99
	ds_write2_b32 v82, v90, v83 offset0:68 offset1:100
	s_waitcnt lgkmcnt(4)
	v_add_f32_e32 v83, v112, v113
	v_fmamk_f32 v83, v83, 0x3c000000, v154
	v_rsq_f32_e32 v83, v83
	v_pk_mul_f32 v[90:91], v[132:133], v[106:107]
	v_pk_fma_f32 v[86:87], v[132:133], v[104:105], v[86:87] neg_lo:[0,0,1] neg_hi:[0,0,1]
	v_pk_fma_f32 v[90:91], v[134:135], v[104:105], v[90:91]
	v_mul_f32_e32 v94, v158, v83
	v_mov_b32_e32 v104, v88
	v_mov_b32_e32 v105, v84
	v_mov_b32_e32 v106, v92
	v_mov_b32_e32 v107, v96
	v_pk_mul_f32 v[104:105], v[104:105], v[94:95] op_sel_hi:[1,0]
	v_pk_mul_f32 v[94:95], v[106:107], v[94:95] op_sel_hi:[1,0]
	v_mov_b32_e32 v96, v93
	v_pk_mul_f32 v[106:107], v[90:91], v[94:95]
	v_mov_b32_e32 v93, v78
	v_pk_fma_f32 v[106:107], v[86:87], v[104:105], v[106:107]
	v_pk_mul_f32 v[104:105], v[90:91], v[104:105]
	v_cvt_pk_f16_f32 v83, v106, v107
	v_pk_fma_f32 v[94:95], v[86:87], v[94:95], v[104:105] neg_lo:[0,0,1] neg_hi:[0,0,1]
	v_mov_b32_e32 v78, v75
	v_cvt_pk_f16_f32 v84, v94, v95
	ds_write2_b32 v82, v83, v84 offset0:136 offset1:168
	s_waitcnt lgkmcnt(3)
	v_add_f32_e32 v83, v115, v119
	v_fmamk_f32 v83, v83, 0x3c000000, v154
	v_rsq_f32_e32 v83, v83
	v_pk_mul_f32 v[94:95], v[134:135], v[90:91]
	v_pk_mul_f32 v[90:91], v[132:133], v[90:91]
	v_mov_b32_e32 v84, v89
	v_mul_f32_e32 v88, v158, v83
	v_pk_fma_f32 v[94:95], v[132:133], v[86:87], v[94:95] neg_lo:[0,0,1] neg_hi:[0,0,1]
	v_pk_fma_f32 v[86:87], v[134:135], v[86:87], v[90:91]
	v_pk_mul_f32 v[84:85], v[84:85], v[88:89] op_sel_hi:[1,0]
	v_pk_mul_f32 v[88:89], v[96:97], v[88:89] op_sel_hi:[1,0]
	s_nop 0
	v_pk_mul_f32 v[90:91], v[86:87], v[88:89]
	s_nop 0
	v_pk_fma_f32 v[90:91], v[94:95], v[84:85], v[90:91]
	v_pk_mul_f32 v[84:85], v[86:87], v[84:85]
	v_cvt_pk_f16_f32 v83, v90, v91
	v_pk_fma_f32 v[84:85], v[94:95], v[88:89], v[84:85] neg_lo:[0,0,1] neg_hi:[0,0,1]
	v_lshlrev_b32_e32 v87, 2, v177
	v_cvt_pk_f16_f32 v84, v84, v85
	ds_write2_b32 v82, v83, v84 offset0:204 offset1:236
	v_lshlrev_b32_e32 v83, 2, v174
	v_or_b32_e32 v86, v83, v1
	v_bitop3_b32 v83, v83, 1, v1 bitop3:0x36
	v_lshlrev_b32_e32 v89, 2, v176
	v_lshlrev_b32_e32 v91, 2, v175
	v_lshl_add_u32 v86, v86, 2, 0
	v_lshl_add_u32 v83, v83, 2, 0
	v_or_b32_e32 v88, v87, v1
	v_bitop3_b32 v87, v87, 1, v1 bitop3:0x36
	v_or_b32_e32 v90, v89, v1
	v_bitop3_b32 v89, v89, 1, v1 bitop3:0x36
	v_or_b32_e32 v92, v91, v1
	v_bitop3_b32 v91, v91, 1, v1 bitop3:0x36
	v_lshl_add_u32 v88, v88, 2, 0
	v_lshl_add_u32 v87, v87, 2, 0
	v_lshl_add_u32 v90, v90, 2, 0
	v_lshl_add_u32 v89, v89, 2, 0
	v_lshl_add_u32 v92, v92, 2, 0
	v_lshl_add_u32 v91, v91, 2, 0
	ds_read_b32 v86, v86
	ds_read_b32 v83, v83
	ds_read_b32 v94, v88
	ds_read_b32 v95, v87
	ds_read_b32 v96, v90
	ds_read_b32 v97, v89
	ds_read_b32 v99, v92
	ds_read_b32 v104, v91
	s_waitcnt lgkmcnt(6)
	v_add_f32_e32 v83, v86, v83
	v_fmamk_f32 v83, v83, 0x3c000000, v154
	v_rsq_f32_e32 v83, v83
	v_pk_mul_f32 v[86:87], v[138:139], v[102:103]
	v_mov_b32_e32 v90, v70
	v_mov_b32_e32 v91, v66
	v_mul_f32_e32 v88, v158, v83
	v_mov_b32_e32 v92, v74
	v_pk_mul_f32 v[84:85], v[140:141], v[102:103]
	v_pk_fma_f32 v[86:87], v[140:141], v[100:101], v[86:87]
	v_pk_mul_f32 v[90:91], v[90:91], v[88:89] op_sel_hi:[1,0]
	v_pk_mul_f32 v[88:89], v[92:93], v[88:89] op_sel_hi:[1,0]
	v_pk_fma_f32 v[84:85], v[138:139], v[100:101], v[84:85] neg_lo:[0,0,1] neg_hi:[0,0,1]
	v_pk_mul_f32 v[92:93], v[86:87], v[88:89]
	v_and_or_b32 v83, v174, s4, v161
	v_pk_fma_f32 v[92:93], v[84:85], v[90:91], v[92:93]
	v_pk_mul_f32 v[90:91], v[86:87], v[90:91]
	v_mad_u32_u24 v83, v83, s0, v162
	v_pk_fma_f32 v[88:89], v[84:85], v[88:89], v[90:91] neg_lo:[0,0,1] neg_hi:[0,0,1]
	v_cvt_pk_f16_f32 v66, v92, v93
	v_cvt_pk_f16_f32 v70, v88, v89
	v_add_u32_e32 v74, 0x1000, v83
	ds_write2_b32 v74, v66, v70 offset1:32
	s_waitcnt lgkmcnt(5)
	v_add_f32_e32 v66, v94, v95
	v_fmamk_f32 v66, v66, 0x3c000000, v154
	v_rsq_f32_e32 v66, v66
	v_pk_mul_f32 v[88:89], v[134:135], v[86:87]
	v_pk_mul_f32 v[86:87], v[132:133], v[86:87]
	v_pk_fma_f32 v[88:89], v[132:133], v[84:85], v[88:89] neg_lo:[0,0,1] neg_hi:[0,0,1]
	v_mul_f32_e32 v70, v158, v66
	v_or_b32_sdwa v66, v161, v130 dst_sel:DWORD dst_unused:UNUSED_PAD src0_sel:DWORD src1_sel:WORD_0
	v_mad_u32_u24 v83, v66, s0, v162
	v_mov_b32_e32 v66, v71
	v_pk_fma_f32 v[84:85], v[134:135], v[84:85], v[86:87]
	v_pk_mul_f32 v[66:67], v[66:67], v[70:71] op_sel_hi:[1,0]
	v_pk_mul_f32 v[70:71], v[78:79], v[70:71] op_sel_hi:[1,0]
	v_mov_b32_e32 v78, v72
	v_pk_mul_f32 v[74:75], v[84:85], v[70:71]
	v_mov_b32_e32 v79, v68
	v_pk_fma_f32 v[74:75], v[88:89], v[66:67], v[74:75]
	v_pk_mul_f32 v[66:67], v[84:85], v[66:67]
	v_cvt_pk_f16_f32 v74, v74, v75
	v_pk_fma_f32 v[66:67], v[88:89], v[70:71], v[66:67] neg_lo:[0,0,1] neg_hi:[0,0,1]
	v_pk_mul_f32 v[70:71], v[134:135], v[84:85]
	v_cvt_pk_f16_f32 v66, v66, v67
	v_add_u32_e32 v67, 0x1000, v83
	ds_write2_b32 v67, v74, v66 offset0:68 offset1:100
	s_waitcnt lgkmcnt(4)
	v_add_f32_e32 v66, v96, v97
	v_fmamk_f32 v66, v66, 0x3c000000, v154
	v_rsq_f32_e32 v66, v66
	v_pk_mul_f32 v[74:75], v[132:133], v[84:85]
	v_mov_b32_e32 v84, v76
	v_mov_b32_e32 v85, v80
	v_mul_f32_e32 v66, v158, v66
	v_pk_fma_f32 v[74:75], v[134:135], v[88:89], v[74:75]
	v_pk_mul_f32 v[84:85], v[84:85], v[66:67] op_sel_hi:[1,0]
	v_pk_fma_f32 v[70:71], v[132:133], v[88:89], v[70:71] neg_lo:[0,0,1] neg_hi:[0,0,1]
	v_pk_mul_f32 v[78:79], v[78:79], v[66:67] op_sel_hi:[1,0]
	v_pk_mul_f32 v[86:87], v[74:75], v[84:85]
	v_mov_b32_e32 v80, v77
	v_pk_fma_f32 v[86:87], v[70:71], v[78:79], v[86:87]
	v_pk_mul_f32 v[78:79], v[74:75], v[78:79]
	v_cvt_pk_f16_f32 v66, v86, v87
	v_pk_fma_f32 v[78:79], v[70:71], v[84:85], v[78:79] neg_lo:[0,0,1] neg_hi:[0,0,1]
	s_nop 0
	v_cvt_pk_f16_f32 v68, v78, v79
	ds_write2_b32 v67, v66, v68 offset0:136 offset1:168
	s_waitcnt lgkmcnt(3)
	v_add_f32_e32 v66, v99, v104
	v_fmamk_f32 v66, v66, 0x3c000000, v154
	v_rsq_f32_e32 v66, v66
	v_pk_mul_f32 v[78:79], v[134:135], v[74:75]
	v_pk_mul_f32 v[74:75], v[132:133], v[74:75]
	v_pk_fma_f32 v[78:79], v[132:133], v[70:71], v[78:79] neg_lo:[0,0,1] neg_hi:[0,0,1]
	v_mul_f32_e32 v66, v158, v66
	v_pk_fma_f32 v[70:71], v[134:135], v[70:71], v[74:75]
	v_mov_b32_e32 v68, v73
	v_pk_mul_f32 v[72:73], v[80:81], v[66:67] op_sel_hi:[1,0]
	v_pk_mul_f32 v[68:69], v[68:69], v[66:67] op_sel_hi:[1,0]
	v_pk_mul_f32 v[74:75], v[70:71], v[72:73]
	s_nop 0
	v_pk_fma_f32 v[74:75], v[78:79], v[68:69], v[74:75]
	v_pk_mul_f32 v[68:69], v[70:71], v[68:69]
	v_cvt_pk_f16_f32 v66, v74, v75
	v_pk_fma_f32 v[68:69], v[78:79], v[72:73], v[68:69] neg_lo:[0,0,1] neg_hi:[0,0,1]
	s_nop 0
	v_cvt_pk_f16_f32 v68, v68, v69
	ds_write2_b32 v67, v66, v68 offset0:204 offset1:236
	s_waitcnt lgkmcnt(0)
	s_barrier
	ds_read_b128 v[70:73], v155 offset:4096
	v_or_b32_e32 v66, s2, v152
	v_lshlrev_b32_e32 v130, 8, v66
	v_or_b32_e32 v66, 0x200, v0
	v_lshrrev_b32_e32 v66, 4, v66
	v_lshl_add_u64 v[78:79], v[136:137], 0, v[130:131]
	v_mad_u32_u24 v68, v66, s0, v182
	v_or_b32_e32 v69, s2, v66
	ds_read_b128 v[74:77], v68 offset:38912
	s_waitcnt lgkmcnt(1)
	global_store_dwordx4 v[78:79], v[70:73], off sc1
	ds_read_b128 v[78:81], v68 offset:4096
	v_lshlrev_b32_e32 v130, 8, v69
	v_or_b32_e32 v69, 64, v152
	v_mad_u32_u24 v70, v69, s0, v182
	ds_read_b128 v[84:87], v70 offset:4096
	v_or_b32_e32 v0, 0x600, v0
	v_or_b32_e32 v71, s2, v69
	v_lshrrev_b32_e32 v0, 4, v0
	v_lshl_add_u64 v[72:73], v[136:137], 0, v[130:131]
	v_lshlrev_b32_e32 v130, 8, v71
	v_mad_u32_u24 v71, v0, s0, v182
	s_waitcnt lgkmcnt(1)
	global_store_dwordx4 v[72:73], v[78:81], off sc1
	ds_read_b128 v[78:81], v71 offset:4096
	v_lshl_add_u64 v[72:73], v[136:137], 0, v[130:131]
	s_waitcnt lgkmcnt(1)
	global_store_dwordx4 v[72:73], v[84:87], off sc1
	v_or_b32_e32 v72, s2, v0
	v_lshlrev_b32_e32 v130, 8, v72
	v_or_b32_e32 v72, 0x80, v0
	v_lshl_add_u64 v[88:89], v[136:137], 0, v[130:131]
	v_mad_u32_u24 v72, v72, s0, v182
	ds_read_b128 v[84:87], v72 offset:4096
	s_waitcnt lgkmcnt(1)
	global_store_dwordx4 v[88:89], v[78:81], off sc1
	ds_read_b128 v[78:81], v155 offset:38912
	v_or_b32_e32 v73, s5, v152
	ds_read_b128 v[88:91], v155 offset:56320
	v_lshlrev_b32_e32 v130, 8, v73
	v_or_b32_e32 v73, s5, v66
	v_lshl_add_u64 v[92:93], v[136:137], 0, v[130:131]
	v_lshlrev_b32_e32 v130, 8, v73
	v_or_b32_e32 v73, s5, v69
	s_waitcnt lgkmcnt(1)
	global_store_dwordx4 v[92:93], v[78:81], off sc1
	s_nop 1
	v_lshl_add_u64 v[78:79], v[136:137], 0, v[130:131]
	v_lshlrev_b32_e32 v130, 8, v73
	v_or_b32_e32 v73, s5, v0
	global_store_dwordx4 v[78:79], v[74:77], off sc1
	v_lshlrev_b32_e32 v79, 2, v170
	v_or_b32_e32 v80, v79, v1
	v_lshl_add_u64 v[74:75], v[136:137], 0, v[130:131]
	v_lshlrev_b32_e32 v130, 8, v73
	s_waitcnt lgkmcnt(0)
	global_store_dwordx4 v[74:75], v[88:91], off sc1
	v_lshl_add_u64 v[74:75], v[136:137], 0, v[130:131]
	v_lshlrev_b32_e32 v73, 2, v173
	global_store_dwordx4 v[74:75], v[84:87], off sc1
	v_or_b32_e32 v74, v73, v1
	v_bitop3_b32 v73, v73, 1, v1 bitop3:0x36
	v_lshlrev_b32_e32 v75, 2, v172
	v_lshlrev_b32_e32 v77, 2, v171
	v_lshl_add_u32 v74, v74, 2, 0
	v_lshl_add_u32 v73, v73, 2, 0
	v_or_b32_e32 v76, v75, v1
	v_bitop3_b32 v75, v75, 1, v1 bitop3:0x36
	v_or_b32_e32 v78, v77, v1
	v_bitop3_b32 v77, v77, 1, v1 bitop3:0x36
	v_bitop3_b32 v79, v79, 1, v1 bitop3:0x36
	s_barrier
	v_lshl_add_u32 v76, v76, 2, 0
	v_lshl_add_u32 v75, v75, 2, 0
	v_lshl_add_u32 v78, v78, 2, 0
	v_lshl_add_u32 v77, v77, 2, 0
	v_lshl_add_u32 v80, v80, 2, 0
	v_lshl_add_u32 v79, v79, 2, 0
	ds_read_b32 v74, v74
	ds_read_b32 v73, v73
	ds_read_b32 v83, v76
	ds_read_b32 v86, v75
	ds_read_b32 v87, v78
	ds_read_b32 v88, v77
	ds_read_b32 v89, v80
	ds_read_b32 v90, v79
	s_waitcnt lgkmcnt(6)
	v_add_f32_e32 v73, v74, v73
	v_fmamk_f32 v73, v73, 0x3c000000, v154
	v_rsq_f32_e32 v73, v73
	v_pk_mul_f32 v[76:77], v[142:143], v[148:149]
	v_mov_b32_e32 v80, v54
	v_mov_b32_e32 v81, v50
	v_mul_f32_e32 v78, v158, v73
	v_mov_b32_e32 v84, v58
	v_mov_b32_e32 v85, v62
	v_pk_fma_f32 v[76:77], v[144:145], v[146:147], v[76:77]
	v_pk_mul_f32 v[80:81], v[80:81], v[78:79] op_sel_hi:[1,0]
	v_pk_mul_f32 v[78:79], v[84:85], v[78:79] op_sel_hi:[1,0]
	v_pk_fma_f32 v[74:75], v[142:143], v[146:147], v[150:151] neg_lo:[0,0,1] neg_hi:[0,0,1]
	v_pk_mul_f32 v[84:85], v[76:77], v[78:79]
	v_mov_b32_e32 v62, v59
	v_pk_fma_f32 v[84:85], v[74:75], v[80:81], v[84:85]
	v_pk_mul_f32 v[80:81], v[76:77], v[80:81]
	v_cvt_pk_f16_f32 v50, v84, v85
	v_pk_fma_f32 v[78:79], v[74:75], v[78:79], v[80:81] neg_lo:[0,0,1] neg_hi:[0,0,1]
	v_pk_mul_f32 v[80:81], v[132:133], v[76:77]
	v_cvt_pk_f16_f32 v54, v78, v79
	ds_write2_b32 v118, v50, v54 offset1:32
	s_waitcnt lgkmcnt(5)
	v_add_f32_e32 v50, v83, v86
	v_fmamk_f32 v50, v50, 0x3c000000, v154
	v_rsq_f32_e32 v50, v50
	v_pk_mul_f32 v[78:79], v[134:135], v[76:77]
	v_pk_fma_f32 v[80:81], v[134:135], v[74:75], v[80:81]
	v_pk_fma_f32 v[78:79], v[132:133], v[74:75], v[78:79] neg_lo:[0,0,1] neg_hi:[0,0,1]
	v_mul_f32_e32 v54, v158, v50
	v_mov_b32_e32 v50, v55
	v_pk_mul_f32 v[50:51], v[50:51], v[54:55] op_sel_hi:[1,0]
	v_pk_mul_f32 v[54:55], v[62:63], v[54:55] op_sel_hi:[1,0]
	v_mov_b32_e32 v62, v56
	v_pk_mul_f32 v[58:59], v[80:81], v[54:55]
	v_mov_b32_e32 v63, v52
	v_pk_fma_f32 v[58:59], v[78:79], v[50:51], v[58:59]
	v_pk_mul_f32 v[50:51], v[80:81], v[50:51]
	v_cvt_pk_f16_f32 v58, v58, v59
	v_pk_fma_f32 v[50:51], v[78:79], v[54:55], v[50:51] neg_lo:[0,0,1] neg_hi:[0,0,1]
	s_waitcnt lgkmcnt(3)
	v_add_f32_e32 v54, v87, v88
	v_cvt_pk_f16_f32 v50, v50, v51
	v_fmamk_f32 v54, v54, 0x3c000000, v154
	ds_write2_b32 v114, v58, v50 offset0:68 offset1:100
	v_rsq_f32_e32 v58, v54
	v_pk_mul_f32 v[50:51], v[134:135], v[80:81]
	v_pk_mul_f32 v[54:55], v[132:133], v[80:81]
	v_pk_fma_f32 v[50:51], v[132:133], v[78:79], v[50:51] neg_lo:[0,0,1] neg_hi:[0,0,1]
	v_pk_fma_f32 v[54:55], v[134:135], v[78:79], v[54:55]
	v_mul_f32_e32 v58, v158, v58
	v_mov_b32_e32 v78, v60
	v_mov_b32_e32 v79, v64
	v_pk_mul_f32 v[62:63], v[62:63], v[58:59] op_sel_hi:[1,0]
	v_pk_mul_f32 v[58:59], v[78:79], v[58:59] op_sel_hi:[1,0]
	v_mov_b32_e32 v64, v61
	v_pk_mul_f32 v[78:79], v[54:55], v[58:59]
	s_nop 0
	v_pk_fma_f32 v[78:79], v[50:51], v[62:63], v[78:79]
	v_pk_mul_f32 v[62:63], v[54:55], v[62:63]
	v_cvt_pk_f16_f32 v52, v78, v79
	v_pk_fma_f32 v[58:59], v[50:51], v[58:59], v[62:63] neg_lo:[0,0,1] neg_hi:[0,0,1]
	s_nop 0
	v_cvt_pk_f16_f32 v56, v58, v59
	ds_write2_b32 v114, v52, v56 offset0:136 offset1:168
	s_waitcnt lgkmcnt(3)
	v_add_f32_e32 v52, v89, v90
	v_fmamk_f32 v52, v52, 0x3c000000, v154
	v_rsq_f32_e32 v52, v52
	v_pk_mul_f32 v[58:59], v[134:135], v[54:55]
	v_pk_mul_f32 v[54:55], v[132:133], v[54:55]
	v_pk_fma_f32 v[58:59], v[132:133], v[50:51], v[58:59] neg_lo:[0,0,1] neg_hi:[0,0,1]
	v_pk_fma_f32 v[50:51], v[134:135], v[50:51], v[54:55]
	v_mul_f32_e32 v54, v158, v52
	v_mov_b32_e32 v52, v57
	v_pk_mul_f32 v[52:53], v[52:53], v[54:55] op_sel_hi:[1,0]
	v_pk_mul_f32 v[54:55], v[64:65], v[54:55] op_sel_hi:[1,0]
	s_nop 0
	v_pk_mul_f32 v[56:57], v[50:51], v[54:55]
	v_pk_mul_f32 v[50:51], v[50:51], v[52:53]
	v_pk_fma_f32 v[56:57], v[58:59], v[52:53], v[56:57]
	v_pk_fma_f32 v[50:51], v[58:59], v[54:55], v[50:51] neg_lo:[0,0,1] neg_hi:[0,0,1]
	v_cvt_pk_f16_f32 v56, v56, v57
	v_cvt_pk_f16_f32 v50, v50, v51
	v_lshlrev_b32_e32 v52, 2, v166
	ds_write2_b32 v114, v56, v50 offset0:204 offset1:236
	v_or_b32_e32 v53, v52, v1
	v_bitop3_b32 v52, v52, 1, v1 bitop3:0x36
	v_lshlrev_b32_e32 v54, 2, v169
	v_lshlrev_b32_e32 v56, 2, v168
	v_lshlrev_b32_e32 v58, 2, v167
	v_lshl_add_u32 v53, v53, 2, 0
	v_lshl_add_u32 v52, v52, 2, 0
	v_or_b32_e32 v55, v54, v1
	v_bitop3_b32 v54, v54, 1, v1 bitop3:0x36
	v_or_b32_e32 v57, v56, v1
	v_bitop3_b32 v56, v56, 1, v1 bitop3:0x36
	v_or_b32_e32 v59, v58, v1
	v_bitop3_b32 v58, v58, 1, v1 bitop3:0x36
	v_lshl_add_u32 v55, v55, 2, 0
	v_lshl_add_u32 v54, v54, 2, 0
	v_lshl_add_u32 v57, v57, 2, 0
	v_lshl_add_u32 v56, v56, 2, 0
	v_lshl_add_u32 v59, v59, 2, 0
	v_lshl_add_u32 v58, v58, 2, 0
	ds_read_b32 v53, v53
	ds_read_b32 v52, v52
	ds_read_b32 v60, v55
	ds_read_b32 v61, v54
	ds_read_b32 v62, v57
	ds_read_b32 v63, v56
	ds_read_b32 v64, v59
	ds_read_b32 v65, v58
	s_waitcnt lgkmcnt(6)
	v_add_f32_e32 v52, v53, v52
	v_fmamk_f32 v52, v52, 0x3c000000, v154
	v_rsq_f32_e32 v54, v52
	v_pk_mul_f32 v[52:53], v[138:139], v[76:77]
	v_and_or_b32 v55, v166, s1, v161
	v_mov_b32_e32 v56, v38
	v_mul_f32_e32 v54, v158, v54
	v_mov_b32_e32 v57, v34
	v_mov_b32_e32 v58, v42
	v_mov_b32_e32 v59, v46
	v_pk_mul_f32 v[50:51], v[140:141], v[76:77]
	v_pk_fma_f32 v[52:53], v[140:141], v[74:75], v[52:53]
	v_mad_u32_u24 v73, v55, s0, v162
	v_pk_mul_f32 v[56:57], v[56:57], v[54:55] op_sel_hi:[1,0]
	v_pk_mul_f32 v[54:55], v[58:59], v[54:55] op_sel_hi:[1,0]
	v_pk_fma_f32 v[50:51], v[138:139], v[74:75], v[50:51] neg_lo:[0,0,1] neg_hi:[0,0,1]
	v_pk_mul_f32 v[58:59], v[52:53], v[54:55]
	v_add_u32_e32 v42, 0x1000, v73
	v_pk_fma_f32 v[58:59], v[50:51], v[56:57], v[58:59]
	v_pk_mul_f32 v[56:57], v[52:53], v[56:57]
	v_cvt_pk_f16_f32 v34, v58, v59
	v_pk_fma_f32 v[54:55], v[50:51], v[54:55], v[56:57] neg_lo:[0,0,1] neg_hi:[0,0,1]
	v_pk_mul_f32 v[56:57], v[132:133], v[52:53]
	v_cvt_pk_f16_f32 v38, v54, v55
	ds_write2_b32 v42, v34, v38 offset1:32
	s_waitcnt lgkmcnt(5)
	v_add_f32_e32 v34, v60, v61
	v_fmamk_f32 v34, v34, 0x3c000000, v154
	v_rsq_f32_e32 v34, v34
	v_mov_b32_e32 v46, v43
	v_pk_mul_f32 v[54:55], v[134:135], v[52:53]
	v_pk_fma_f32 v[56:57], v[134:135], v[50:51], v[56:57]
	v_mul_f32_e32 v38, v158, v34
	v_mov_b32_e32 v34, v39
	v_pk_mul_f32 v[34:35], v[34:35], v[38:39] op_sel_hi:[1,0]
	v_pk_mul_f32 v[38:39], v[46:47], v[38:39] op_sel_hi:[1,0]
	v_pk_fma_f32 v[54:55], v[132:133], v[50:51], v[54:55] neg_lo:[0,0,1] neg_hi:[0,0,1]
	v_pk_mul_f32 v[42:43], v[56:57], v[38:39]
	v_mov_b32_e32 v46, v40
	v_pk_fma_f32 v[42:43], v[54:55], v[34:35], v[42:43]
	v_pk_mul_f32 v[34:35], v[56:57], v[34:35]
	v_cvt_pk_f16_f32 v42, v42, v43
	v_pk_fma_f32 v[34:35], v[54:55], v[38:39], v[34:35] neg_lo:[0,0,1] neg_hi:[0,0,1]
	s_waitcnt lgkmcnt(3)
	v_add_f32_e32 v38, v62, v63
	v_cvt_pk_f16_f32 v34, v34, v35
	v_fmamk_f32 v38, v38, 0x3c000000, v154
	ds_write2_b32 v98, v42, v34 offset0:68 offset1:100
	v_rsq_f32_e32 v42, v38
	v_pk_mul_f32 v[34:35], v[134:135], v[56:57]
	v_pk_mul_f32 v[38:39], v[132:133], v[56:57]
	v_pk_fma_f32 v[34:35], v[132:133], v[54:55], v[34:35] neg_lo:[0,0,1] neg_hi:[0,0,1]
	v_pk_fma_f32 v[38:39], v[134:135], v[54:55], v[38:39]
	v_mul_f32_e32 v42, v158, v42
	v_mov_b32_e32 v47, v36
	v_mov_b32_e32 v54, v44
	v_mov_b32_e32 v55, v48
	v_pk_mul_f32 v[46:47], v[46:47], v[42:43] op_sel_hi:[1,0]
	v_pk_mul_f32 v[42:43], v[54:55], v[42:43] op_sel_hi:[1,0]
	v_mov_b32_e32 v48, v45
	v_pk_mul_f32 v[54:55], v[38:39], v[42:43]
	s_nop 0
	v_pk_fma_f32 v[54:55], v[34:35], v[46:47], v[54:55]
	v_pk_mul_f32 v[46:47], v[38:39], v[46:47]
	v_cvt_pk_f16_f32 v36, v54, v55
	v_pk_fma_f32 v[42:43], v[34:35], v[42:43], v[46:47] neg_lo:[0,0,1] neg_hi:[0,0,1]
	s_nop 0
	v_cvt_pk_f16_f32 v40, v42, v43
	ds_write2_b32 v98, v36, v40 offset0:136 offset1:168
	s_waitcnt lgkmcnt(3)
	v_add_f32_e32 v36, v64, v65
	v_fmamk_f32 v36, v36, 0x3c000000, v154
	v_rsq_f32_e32 v36, v36
	v_pk_mul_f32 v[42:43], v[134:135], v[38:39]
	v_pk_mul_f32 v[38:39], v[132:133], v[38:39]
	v_pk_fma_f32 v[42:43], v[132:133], v[34:35], v[42:43] neg_lo:[0,0,1] neg_hi:[0,0,1]
	v_pk_fma_f32 v[34:35], v[134:135], v[34:35], v[38:39]
	v_mul_f32_e32 v38, v158, v36
	v_mov_b32_e32 v36, v41
	v_pk_mul_f32 v[36:37], v[36:37], v[38:39] op_sel_hi:[1,0]
	v_pk_mul_f32 v[38:39], v[48:49], v[38:39] op_sel_hi:[1,0]
	s_nop 0
	v_pk_mul_f32 v[40:41], v[34:35], v[38:39]
	v_pk_mul_f32 v[34:35], v[34:35], v[36:37]
	v_pk_fma_f32 v[40:41], v[42:43], v[36:37], v[40:41]
	v_pk_fma_f32 v[34:35], v[42:43], v[38:39], v[34:35] neg_lo:[0,0,1] neg_hi:[0,0,1]
	v_cvt_pk_f16_f32 v40, v40, v41
	v_cvt_pk_f16_f32 v34, v34, v35
	v_lshlrev_b32_e32 v36, 2, v160
	ds_write2_b32 v98, v40, v34 offset0:204 offset1:236
	v_or_b32_e32 v37, v36, v1
	v_bitop3_b32 v36, v36, 1, v1 bitop3:0x36
	v_lshlrev_b32_e32 v38, 2, v165
	v_lshlrev_b32_e32 v40, 2, v164
	v_lshlrev_b32_e32 v42, 2, v163
	v_lshl_add_u32 v37, v37, 2, 0
	v_lshl_add_u32 v36, v36, 2, 0
	v_or_b32_e32 v39, v38, v1
	v_bitop3_b32 v38, v38, 1, v1 bitop3:0x36
	v_or_b32_e32 v41, v40, v1
	v_bitop3_b32 v40, v40, 1, v1 bitop3:0x36
	v_or_b32_e32 v43, v42, v1
	v_bitop3_b32 v42, v42, 1, v1 bitop3:0x36
	v_lshl_add_u32 v39, v39, 2, 0
	v_lshl_add_u32 v38, v38, 2, 0
	v_lshl_add_u32 v41, v41, 2, 0
	v_lshl_add_u32 v40, v40, 2, 0
	v_lshl_add_u32 v43, v43, 2, 0
	v_lshl_add_u32 v42, v42, 2, 0
	ds_read_b32 v37, v37
	ds_read_b32 v36, v36
	ds_read_b32 v44, v39
	ds_read_b32 v45, v38
	ds_read_b32 v46, v41
	ds_read_b32 v47, v40
	ds_read_b32 v48, v43
	ds_read_b32 v49, v42
	s_waitcnt lgkmcnt(6)
	v_add_f32_e32 v36, v37, v36
	v_fmamk_f32 v36, v36, 0x3c000000, v154
	v_rsq_f32_e32 v38, v36
	v_pk_mul_f32 v[34:35], v[140:141], v[52:53]
	v_pk_mul_f32 v[36:37], v[138:139], v[52:53]
	v_and_or_b32 v39, v160, s3, v161
	v_mul_f32_e32 v38, v158, v38
	v_mov_b32_e32 v40, v22
	v_mov_b32_e32 v41, v18
	v_mov_b32_e32 v42, v26
	v_mov_b32_e32 v43, v30
	v_pk_fma_f32 v[34:35], v[138:139], v[50:51], v[34:35] neg_lo:[0,0,1] neg_hi:[0,0,1]
	v_pk_fma_f32 v[36:37], v[140:141], v[50:51], v[36:37]
	v_mad_u32_u24 v50, v39, s0, v162
	v_pk_mul_f32 v[40:41], v[40:41], v[38:39] op_sel_hi:[1,0]
	v_pk_mul_f32 v[38:39], v[42:43], v[38:39] op_sel_hi:[1,0]
	v_add_u32_e32 v26, 0x1000, v50
	v_pk_mul_f32 v[42:43], v[36:37], v[38:39]
	v_mov_b32_e32 v30, v27
	v_pk_fma_f32 v[42:43], v[34:35], v[40:41], v[42:43]
	v_pk_mul_f32 v[40:41], v[36:37], v[40:41]
	v_cvt_pk_f16_f32 v18, v42, v43
	v_pk_fma_f32 v[38:39], v[34:35], v[38:39], v[40:41] neg_lo:[0,0,1] neg_hi:[0,0,1]
	v_pk_mul_f32 v[40:41], v[132:133], v[36:37]
	v_cvt_pk_f16_f32 v22, v38, v39
	ds_write2_b32 v26, v18, v22 offset1:32
	s_waitcnt lgkmcnt(5)
	v_add_f32_e32 v18, v44, v45
	v_fmamk_f32 v18, v18, 0x3c000000, v154
	v_rsq_f32_e32 v18, v18
	v_pk_mul_f32 v[38:39], v[134:135], v[36:37]
	v_pk_fma_f32 v[40:41], v[134:135], v[34:35], v[40:41]
	v_pk_fma_f32 v[38:39], v[132:133], v[34:35], v[38:39] neg_lo:[0,0,1] neg_hi:[0,0,1]
	v_mul_f32_e32 v22, v158, v18
	v_mov_b32_e32 v18, v23
	v_pk_mul_f32 v[18:19], v[18:19], v[22:23] op_sel_hi:[1,0]
	v_pk_mul_f32 v[22:23], v[30:31], v[22:23] op_sel_hi:[1,0]
	v_mov_b32_e32 v30, v24
	v_pk_mul_f32 v[26:27], v[40:41], v[22:23]
	v_mov_b32_e32 v31, v20
	v_pk_fma_f32 v[26:27], v[38:39], v[18:19], v[26:27]
	v_pk_mul_f32 v[18:19], v[40:41], v[18:19]
	v_cvt_pk_f16_f32 v26, v26, v27
	v_pk_fma_f32 v[18:19], v[38:39], v[22:23], v[18:19] neg_lo:[0,0,1] neg_hi:[0,0,1]
	s_waitcnt lgkmcnt(3)
	v_add_f32_e32 v22, v46, v47
	v_cvt_pk_f16_f32 v18, v18, v19
	v_fmamk_f32 v22, v22, 0x3c000000, v154
	ds_write2_b32 v82, v26, v18 offset0:68 offset1:100
	v_rsq_f32_e32 v26, v22
	v_pk_mul_f32 v[18:19], v[134:135], v[40:41]
	v_pk_mul_f32 v[22:23], v[132:133], v[40:41]
	v_pk_fma_f32 v[18:19], v[132:133], v[38:39], v[18:19] neg_lo:[0,0,1] neg_hi:[0,0,1]
	v_pk_fma_f32 v[22:23], v[134:135], v[38:39], v[22:23]
	v_mul_f32_e32 v26, v158, v26
	v_mov_b32_e32 v38, v28
	v_mov_b32_e32 v39, v32
	v_pk_mul_f32 v[30:31], v[30:31], v[26:27] op_sel_hi:[1,0]
	v_pk_mul_f32 v[26:27], v[38:39], v[26:27] op_sel_hi:[1,0]
	v_mov_b32_e32 v32, v29
	v_pk_mul_f32 v[38:39], v[22:23], v[26:27]
	s_nop 0
	v_pk_fma_f32 v[38:39], v[18:19], v[30:31], v[38:39]
	v_pk_mul_f32 v[30:31], v[22:23], v[30:31]
	v_cvt_pk_f16_f32 v20, v38, v39
	v_pk_fma_f32 v[26:27], v[18:19], v[26:27], v[30:31] neg_lo:[0,0,1] neg_hi:[0,0,1]
	s_nop 0
	v_cvt_pk_f16_f32 v24, v26, v27
	ds_write2_b32 v82, v20, v24 offset0:136 offset1:168
	s_waitcnt lgkmcnt(3)
	v_add_f32_e32 v20, v48, v49
	v_fmamk_f32 v20, v20, 0x3c000000, v154
	v_rsq_f32_e32 v20, v20
	v_pk_mul_f32 v[26:27], v[134:135], v[22:23]
	v_pk_mul_f32 v[22:23], v[132:133], v[22:23]
	v_pk_fma_f32 v[26:27], v[132:133], v[18:19], v[26:27] neg_lo:[0,0,1] neg_hi:[0,0,1]
	v_pk_fma_f32 v[18:19], v[134:135], v[18:19], v[22:23]
	v_mul_f32_e32 v22, v158, v20
	v_mov_b32_e32 v20, v25
	v_pk_mul_f32 v[20:21], v[20:21], v[22:23] op_sel_hi:[1,0]
	v_pk_mul_f32 v[22:23], v[32:33], v[22:23] op_sel_hi:[1,0]
	s_nop 0
	v_pk_mul_f32 v[24:25], v[18:19], v[22:23]
	v_pk_mul_f32 v[18:19], v[18:19], v[20:21]
	v_pk_fma_f32 v[24:25], v[26:27], v[20:21], v[24:25]
	v_pk_fma_f32 v[18:19], v[26:27], v[22:23], v[18:19] neg_lo:[0,0,1] neg_hi:[0,0,1]
	v_cvt_pk_f16_f32 v24, v24, v25
	v_cvt_pk_f16_f32 v18, v18, v19
	ds_write2_b32 v82, v24, v18 offset0:204 offset1:236
	v_lshlrev_b32_e32 v20, 2, v153
	v_lshlrev_b32_e32 v22, 2, v159
	v_lshlrev_b32_e32 v24, 2, v157
	v_lshlrev_b32_e32 v26, 2, v156
	v_or_b32_e32 v21, v20, v1
	v_bitop3_b32 v20, v20, 1, v1 bitop3:0x36
	v_or_b32_e32 v23, v22, v1
	v_bitop3_b32 v22, v22, 1, v1 bitop3:0x36
	v_or_b32_e32 v25, v24, v1
	v_bitop3_b32 v24, v24, 1, v1 bitop3:0x36
	v_or_b32_e32 v27, v26, v1
	v_bitop3_b32 v1, v26, 1, v1 bitop3:0x36
	v_lshl_add_u32 v21, v21, 2, 0
	v_lshl_add_u32 v20, v20, 2, 0
	v_lshl_add_u32 v1, v1, 2, 0
	v_lshl_add_u32 v23, v23, 2, 0
	v_lshl_add_u32 v22, v22, 2, 0
	v_lshl_add_u32 v25, v25, 2, 0
	v_lshl_add_u32 v24, v24, 2, 0
	v_lshl_add_u32 v27, v27, 2, 0
	ds_read_b32 v21, v21
	ds_read_b32 v20, v20
	ds_read_b32 v28, v23
	ds_read_b32 v29, v22
	ds_read_b32 v30, v25
	ds_read_b32 v31, v24
	ds_read_b32 v32, v27
	ds_read_b32 v1, v1
	s_waitcnt lgkmcnt(6)
	v_add_f32_e32 v20, v21, v20
	v_fmamk_f32 v20, v20, 0x3c000000, v154
	v_rsq_f32_e32 v22, v20
	v_pk_mul_f32 v[20:21], v[138:139], v[36:37]
	v_and_or_b32 v23, v153, s4, v161
	v_mov_b32_e32 v24, v6
	v_mul_f32_e32 v22, v158, v22
	v_mov_b32_e32 v25, v2
	v_mov_b32_e32 v26, v10
	v_mov_b32_e32 v27, v14
	v_pk_mul_f32 v[18:19], v[140:141], v[36:37]
	v_pk_fma_f32 v[20:21], v[140:141], v[34:35], v[20:21]
	v_mad_u32_u24 v33, v23, s0, v162
	v_pk_mul_f32 v[24:25], v[24:25], v[22:23] op_sel_hi:[1,0]
	v_pk_mul_f32 v[22:23], v[26:27], v[22:23] op_sel_hi:[1,0]
	v_pk_fma_f32 v[18:19], v[138:139], v[34:35], v[18:19] neg_lo:[0,0,1] neg_hi:[0,0,1]
	v_pk_mul_f32 v[26:27], v[20:21], v[22:23]
	v_add_u32_e32 v10, 0x1000, v33
	v_pk_fma_f32 v[26:27], v[18:19], v[24:25], v[26:27]
	v_pk_mul_f32 v[24:25], v[20:21], v[24:25]
	v_cvt_pk_f16_f32 v2, v26, v27
	v_pk_fma_f32 v[22:23], v[18:19], v[22:23], v[24:25] neg_lo:[0,0,1] neg_hi:[0,0,1]
	v_mov_b32_e32 v14, v11
	v_cvt_pk_f16_f32 v6, v22, v23
	ds_write2_b32 v10, v2, v6 offset1:32
	s_waitcnt lgkmcnt(5)
	v_add_f32_e32 v2, v28, v29
	v_fmamk_f32 v2, v2, 0x3c000000, v154
	v_rsq_f32_e32 v2, v2
	v_pk_mul_f32 v[22:23], v[134:135], v[20:21]
	v_pk_mul_f32 v[20:21], v[132:133], v[20:21]
	v_pk_fma_f32 v[22:23], v[132:133], v[18:19], v[22:23] neg_lo:[0,0,1] neg_hi:[0,0,1]
	v_mul_f32_e32 v6, v158, v2
	v_mov_b32_e32 v2, v7
	v_pk_fma_f32 v[18:19], v[134:135], v[18:19], v[20:21]
	v_pk_mul_f32 v[2:3], v[2:3], v[6:7] op_sel_hi:[1,0]
	v_pk_mul_f32 v[6:7], v[14:15], v[6:7] op_sel_hi:[1,0]
	v_mov_b32_e32 v14, v8
	v_pk_mul_f32 v[10:11], v[18:19], v[6:7]
	v_mov_b32_e32 v15, v4
	v_pk_fma_f32 v[10:11], v[22:23], v[2:3], v[10:11]
	v_pk_mul_f32 v[2:3], v[18:19], v[2:3]
	v_cvt_pk_f16_f32 v10, v10, v11
	v_pk_fma_f32 v[2:3], v[22:23], v[6:7], v[2:3] neg_lo:[0,0,1] neg_hi:[0,0,1]
	s_waitcnt lgkmcnt(3)
	v_add_f32_e32 v6, v30, v31
	v_cvt_pk_f16_f32 v2, v2, v3
	v_fmamk_f32 v6, v6, 0x3c000000, v154
	ds_write2_b32 v67, v10, v2 offset0:68 offset1:100
	v_rsq_f32_e32 v10, v6
	v_pk_mul_f32 v[2:3], v[134:135], v[18:19]
	v_pk_mul_f32 v[6:7], v[132:133], v[18:19]
	v_mov_b32_e32 v18, v12
	v_mul_f32_e32 v10, v158, v10
	v_mov_b32_e32 v19, v16
	s_waitcnt lgkmcnt(2)
	v_add_f32_e32 v1, v32, v1
	v_pk_fma_f32 v[6:7], v[134:135], v[22:23], v[6:7]
	v_pk_mul_f32 v[14:15], v[14:15], v[10:11] op_sel_hi:[1,0]
	v_pk_mul_f32 v[10:11], v[18:19], v[10:11] op_sel_hi:[1,0]
	v_fmac_f32_e32 v154, 0x3c000000, v1
	v_pk_fma_f32 v[2:3], v[132:133], v[22:23], v[2:3] neg_lo:[0,0,1] neg_hi:[0,0,1]
	v_pk_mul_f32 v[18:19], v[6:7], v[10:11]
	v_rsq_f32_e32 v1, v154
	v_pk_fma_f32 v[18:19], v[2:3], v[14:15], v[18:19]
	v_pk_mul_f32 v[14:15], v[6:7], v[14:15]
	v_cvt_pk_f16_f32 v4, v18, v19
	v_pk_fma_f32 v[10:11], v[2:3], v[10:11], v[14:15] neg_lo:[0,0,1] neg_hi:[0,0,1]
	v_mov_b32_e32 v16, v13
	v_cvt_pk_f16_f32 v8, v10, v11
	v_pk_mul_f32 v[10:11], v[134:135], v[6:7]
	v_pk_mul_f32 v[6:7], v[132:133], v[6:7]
	ds_write2_b32 v67, v4, v8 offset0:136 offset1:168
	v_pk_fma_f32 v[10:11], v[132:133], v[2:3], v[10:11] neg_lo:[0,0,1] neg_hi:[0,0,1]
	v_pk_fma_f32 v[2:3], v[134:135], v[2:3], v[6:7]
	v_mul_f32_e32 v6, v158, v1
	v_mov_b32_e32 v4, v9
	v_pk_mul_f32 v[4:5], v[4:5], v[6:7] op_sel_hi:[1,0]
	v_pk_mul_f32 v[6:7], v[16:17], v[6:7] op_sel_hi:[1,0]
	s_or_b32 s0, s2, 0x80
	v_pk_mul_f32 v[8:9], v[2:3], v[6:7]
	v_pk_mul_f32 v[2:3], v[2:3], v[4:5]
	v_pk_fma_f32 v[8:9], v[10:11], v[4:5], v[8:9]
	v_pk_fma_f32 v[2:3], v[10:11], v[6:7], v[2:3] neg_lo:[0,0,1] neg_hi:[0,0,1]
	v_cvt_pk_f16_f32 v1, v8, v9
	v_cvt_pk_f16_f32 v2, v2, v3
	ds_write2_b32 v67, v1, v2 offset0:204 offset1:236
	s_waitcnt lgkmcnt(0)
	s_barrier
	ds_read_b128 v[2:5], v155 offset:4096
	v_or_b32_e32 v1, s0, v152
	v_lshlrev_b32_e32 v130, 8, v1
	v_lshl_add_u64 v[10:11], v[136:137], 0, v[130:131]
	ds_read_b128 v[6:9], v68 offset:38912
	s_waitcnt lgkmcnt(1)
	global_store_dwordx4 v[10:11], v[2:5], off sc1
	ds_read_b128 v[2:5], v68 offset:4096
	ds_read_b128 v[10:13], v70 offset:4096
	v_or_b32_e32 v1, s0, v66
	v_lshlrev_b32_e32 v130, 8, v1
	v_or_b32_e32 v1, s0, v69
	v_lshl_add_u64 v[14:15], v[136:137], 0, v[130:131]
	v_lshlrev_b32_e32 v130, 8, v1
	s_waitcnt lgkmcnt(1)
	global_store_dwordx4 v[14:15], v[2:5], off sc1
	v_or_b32_e32 v1, s0, v0
	s_or_b32 s0, s2, 0x1080
	v_lshl_add_u64 v[2:3], v[136:137], 0, v[130:131]
	s_waitcnt lgkmcnt(0)
	global_store_dwordx4 v[2:3], v[10:13], off sc1
	ds_read_b128 v[2:5], v71 offset:4096
	ds_read_b128 v[10:13], v72 offset:4096
	v_lshlrev_b32_e32 v130, 8, v1
	v_lshl_add_u64 v[14:15], v[136:137], 0, v[130:131]
	v_or_b32_e32 v1, s0, v152
	s_waitcnt lgkmcnt(1)
	global_store_dwordx4 v[14:15], v[2:5], off sc1
	ds_read_b128 v[2:5], v155 offset:38912
	ds_read_b128 v[14:17], v155 offset:56320
	v_lshlrev_b32_e32 v130, 8, v1
	v_or_b32_e32 v1, s0, v66
	v_lshl_add_u64 v[18:19], v[136:137], 0, v[130:131]
	v_lshlrev_b32_e32 v130, 8, v1
	v_or_b32_e32 v1, s0, v69
	s_waitcnt lgkmcnt(1)
	global_store_dwordx4 v[18:19], v[2:5], off sc1
	v_or_b32_e32 v0, s0, v0
	s_nop 0
	v_lshl_add_u64 v[2:3], v[136:137], 0, v[130:131]
	v_lshlrev_b32_e32 v130, 8, v1
	global_store_dwordx4 v[2:3], v[6:9], off sc1
	v_lshl_add_u64 v[2:3], v[136:137], 0, v[130:131]
	v_lshlrev_b32_e32 v130, 8, v0
	v_lshl_add_u64 v[0:1], v[136:137], 0, v[130:131]
	s_waitcnt lgkmcnt(0)
	global_store_dwordx4 v[2:3], v[14:17], off sc1
	global_store_dwordx4 v[0:1], v[10:13], off sc1
	s_barrier
	s_endpgm

	.amdhsa_kernel _Z8gemm_qkvPKDF16_S0_7EpiArgs
		.amdhsa_group_segment_fixed_size 0
		.amdhsa_private_segment_fixed_size 0
		.amdhsa_kernarg_size 72
		.amdhsa_user_sgpr_count 2
		.amdhsa_user_sgpr_dispatch_ptr 0
		.amdhsa_user_sgpr_queue_ptr 0
		.amdhsa_user_sgpr_kernarg_segment_ptr 1
		.amdhsa_user_sgpr_dispatch_id 0
		.amdhsa_user_sgpr_kernarg_preload_length 0
		.amdhsa_user_sgpr_kernarg_preload_offset 0
		.amdhsa_user_sgpr_private_segment_size 0
		.amdhsa_uses_dynamic_stack 0
		.amdhsa_enable_private_segment 0
		.amdhsa_system_sgpr_workgroup_id_x 1
		.amdhsa_system_sgpr_workgroup_id_y 0
		.amdhsa_system_sgpr_workgroup_id_z 0
		.amdhsa_system_sgpr_workgroup_info 0
		.amdhsa_system_vgpr_workitem_id 0
		.amdhsa_next_free_vgpr 256
		.amdhsa_next_free_sgpr 56
		.amdhsa_accum_offset 256
		.amdhsa_reserve_vcc 1
		.amdhsa_float_round_mode_32 0
		.amdhsa_float_round_mode_16_64 0
		.amdhsa_float_denorm_mode_32 3
		.amdhsa_float_denorm_mode_16_64 3
		.amdhsa_dx10_clamp 1
		.amdhsa_ieee_mode 1
		.amdhsa_fp16_overflow 0
		.amdhsa_tg_split 0
		.amdhsa_exception_fp_ieee_invalid_op 0
		.amdhsa_exception_fp_denorm_src 0
		.amdhsa_exception_fp_ieee_div_zero 0
		.amdhsa_exception_fp_ieee_overflow 0
		.amdhsa_exception_fp_ieee_underflow 0
		.amdhsa_exception_fp_ieee_inexact 0
		.amdhsa_exception_int_div_zero 0
	.end_amdhsa_kernel
